# m11 with XP5 64 (compromise for other tile counts)
# baseline (speedup 1.0000x reference)
; #define LAS __attribute__((address_space(3)))
; __device__ __forceinline__ void cvt_item_lds(const float* src, int ld_src, fp8_t* dst, int ld_dst, LAS unsigned char* lds, int tid, int wv) {
;     const int lane = tid & 63;
;     const float* s = src + (size_t)(16 * wv) * ld_src + 4 * lane;
;     f32x4 va[16], vb[16];
;     cvt8_load(va, s, ld_src);
; #pragma unroll
;     for (int t = 0; t < 8; t += 2) {
;         cvt8_load(vb, s + (t + 1) * 256, ld_src); __builtin_amdgcn_sched_barrier(0);
; __device__ __forceinline__ void conv_queue(const Params& p, LAS unsigned char* lds, const int wave, const int cw, const int first, const int last, const int slot_off = LDS_MISC) {
;     ...
;     for (;;) {
;         __syncthreads();
;         if (tid == 0) *slot = first + (int)atomicAdd(&p.ctl[cw], 1u);
;         __syncthreads();
;         const int it = *slot;
;         if (it >= last) break;
;         if (it < N_GU) { const int e = it >> 5, rem = it & 31, kb = rem >> 1, nh = rem & 1;
;             const float* src = p.w_gu + (size_t)e * ND * (2 * DFF) + (size_t)(kb * 128) * (2 * DFF) + nh * 2048;
;             fp8_t* dst = p.wt_gu + (size_t)e * (2 * DFF) * ND + (size_t)(nh * 2048) * ND + kb * 128;
;             cvt_item_lds(src, 2 * DFF, dst, ND, lds, tid, wave); }
;         else { const int j = it - N_GU, e = j >> 4, kb = j & 15;
;             const float* src = p.w_down + (size_t)e * DFF * ND + (size_t)(kb * 128) * ND;
;             fp8_t* dst = p.wt_down + (size_t)e * ND * DFF + kb * 128;
;             cvt_item_lds(src, ND, dst, DFF, lds, tid, wave); }
.LBB0_822:
	s_or_b64 exec, exec, s[48:49]
	s_waitcnt lgkmcnt(0)
	s_barrier
	ds_read_b32 v0, v209
	s_movk_i32 s2, 0x43f
	s_mov_b64 s[48:49], -1
	s_waitcnt lgkmcnt(0)
	v_cmp_lt_i32_e32 vcc, s2, v0
	v_readfirstlane_b32 s33, v0
	s_cbranch_vccnz .LBB0_817
	s_cmpk_gt_i32 s33, 0x3ff
	s_cbranch_scc0 .LBB0_825
	s_add_i32 s2, s33, 0xfffffc00
	s_lshr_b32 s4, s2, 4
	v_readlane_b32 s16, v254, 22
	s_lshl_b64 s[34:35], s[4:5], 22
	s_lshl_b64 s[48:49], s[4:5], 24
	v_readlane_b32 s20, v254, 26
	v_readlane_b32 s21, v254, 27
	s_add_u32 s2, s20, s48
	s_addc_u32 s4, s21, s49
	s_lshl_b32 s48, s33, 7
	s_and_b32 s48, s48, 0x780
	s_lshl_b32 s49, s48, 13
	s_add_u32 s2, s2, s49
	s_addc_u32 s4, s4, 0
	s_add_u32 s34, s56, s34
	s_addc_u32 s35, s57, s35
	s_add_u32 s50, s34, s48
	s_addc_u32 s51, s35, 0
	s_add_u32 s48, s2, s14
	s_addc_u32 s49, s4, s15
	v_lshl_add_u64 v[172:173], s[48:49], 0, v[128:129]
	s_movk_i32 s2, 0x2000
	v_add_co_u32_e32 v174, vcc, s2, v172
	s_movk_i32 s2, 0x3000
	s_nop 0
	v_addc_co_u32_e32 v175, vcc, 0, v173, vcc
	v_add_co_u32_e32 v142, vcc, s2, v172
	s_movk_i32 s2, 0x6000
	s_nop 0
	v_addc_co_u32_e32 v143, vcc, 0, v173, vcc
	v_add_co_u32_e32 v176, vcc, s13, v172
	v_readlane_b32 s17, v254, 23
	s_nop 0
	v_addc_co_u32_e32 v177, vcc, 0, v173, vcc
	v_add_co_u32_e32 v144, vcc, s67, v172
	v_readlane_b32 s18, v254, 24
	s_nop 0
	v_addc_co_u32_e32 v145, vcc, 0, v173, vcc
	v_add_co_u32_e32 v178, vcc, s2, v172
	s_movk_i32 s2, 0x7000
	s_nop 0
	v_addc_co_u32_e32 v179, vcc, 0, v173, vcc
	v_add_co_u32_e32 v146, vcc, s2, v172
	s_mov_b32 s2, 0xa000
	s_nop 0
	v_addc_co_u32_e32 v147, vcc, 0, v173, vcc
	v_add_co_u32_e32 v180, vcc, s60, v172
	global_load_dwordx4 v[16:19], v[144:145], off offset:-4096 nt
	global_load_dwordx4 v[20:23], v[146:147], off offset:-4096 nt
	v_addc_co_u32_e32 v181, vcc, 0, v173, vcc
	v_add_co_u32_e32 v148, vcc, s68, v172
	v_readlane_b32 s19, v254, 25
	s_nop 0
	v_addc_co_u32_e32 v149, vcc, 0, v173, vcc
	v_add_co_u32_e32 v182, vcc, s2, v172
	s_mov_b32 s2, 0xb000
	s_nop 0
	v_addc_co_u32_e32 v183, vcc, 0, v173, vcc
	v_add_co_u32_e32 v150, vcc, s2, v172
	s_mov_b32 s2, 0xe000
	s_nop 0
	v_addc_co_u32_e32 v151, vcc, 0, v173, vcc
	v_add_co_u32_e32 v184, vcc, s61, v172
	global_load_dwordx4 v[24:27], v[148:149], off offset:-4096 nt
	global_load_dwordx4 v[28:31], v[150:151], off offset:-4096 nt
	v_addc_co_u32_e32 v185, vcc, 0, v173, vcc
	v_add_co_u32_e32 v152, vcc, s69, v172
	v_readlane_b32 s22, v254, 28
	s_nop 0
	v_addc_co_u32_e32 v153, vcc, 0, v173, vcc
	v_add_co_u32_e32 v186, vcc, s2, v172
	s_mov_b32 s2, 0xf000
	s_nop 0
	v_addc_co_u32_e32 v187, vcc, 0, v173, vcc
	v_add_co_u32_e32 v154, vcc, s2, v172
	s_mov_b32 s2, 0x12000
	s_nop 0
	v_addc_co_u32_e32 v155, vcc, 0, v173, vcc
	v_add_co_u32_e32 v188, vcc, s62, v172
	global_load_dwordx4 v[56:59], v[152:153], off offset:-4096 nt
	global_load_dwordx4 v[60:63], v[154:155], off offset:-4096 nt
	v_addc_co_u32_e32 v189, vcc, 0, v173, vcc
	v_add_co_u32_e32 v156, vcc, s88, v172
	v_readlane_b32 s23, v254, 29
	s_nop 0
	v_addc_co_u32_e32 v157, vcc, 0, v173, vcc
	v_add_co_u32_e32 v190, vcc, s2, v172
	s_mov_b32 s2, 0x13000
	s_nop 0
	v_addc_co_u32_e32 v191, vcc, 0, v173, vcc
	v_add_co_u32_e32 v158, vcc, s2, v172
	s_mov_b32 s2, 0x16000
	s_nop 0
	v_addc_co_u32_e32 v159, vcc, 0, v173, vcc
	v_add_co_u32_e32 v192, vcc, s63, v172
	global_load_dwordx4 v[48:51], v[156:157], off offset:-4096 nt
	global_load_dwordx4 v[52:55], v[158:159], off offset:-4096 nt
	v_addc_co_u32_e32 v193, vcc, 0, v173, vcc
	v_add_co_u32_e32 v160, vcc, s89, v172
	v_readlane_b32 s24, v254, 30
	s_nop 0
	v_addc_co_u32_e32 v161, vcc, 0, v173, vcc
	v_add_co_u32_e32 v194, vcc, s2, v172
	s_mov_b32 s2, 0x17000
	s_nop 0
	v_addc_co_u32_e32 v195, vcc, 0, v173, vcc
	v_add_co_u32_e32 v162, vcc, s2, v172
	s_mov_b32 s2, 0x1a000
	s_nop 0
	v_addc_co_u32_e32 v163, vcc, 0, v173, vcc
	v_add_co_u32_e32 v196, vcc, s64, v172
	global_load_dwordx4 v[80:83], v[160:161], off offset:-4096 nt
	global_load_dwordx4 v[84:87], v[162:163], off offset:-4096 nt
	v_addc_co_u32_e32 v197, vcc, 0, v173, vcc
	v_add_co_u32_e32 v164, vcc, s90, v172
	v_readlane_b32 s25, v254, 31
	s_nop 0
	v_addc_co_u32_e32 v165, vcc, 0, v173, vcc
	v_add_co_u32_e32 v198, vcc, s2, v172
	s_mov_b32 s2, 0x1b000
	s_nop 0
	v_addc_co_u32_e32 v199, vcc, 0, v173, vcc
	v_add_co_u32_e32 v166, vcc, s2, v172
	s_mov_b32 s2, 0x1e000
	s_nop 0
	v_addc_co_u32_e32 v167, vcc, 0, v173, vcc
	v_add_co_u32_e32 v200, vcc, s65, v172
	global_load_dwordx4 v[88:91], v[164:165], off offset:-4096 nt
	global_load_dwordx4 v[92:95], v[166:167], off offset:-4096 nt
	v_addc_co_u32_e32 v201, vcc, 0, v173, vcc
	v_add_co_u32_e32 v168, vcc, s91, v172
	v_readlane_b32 s26, v254, 32
	s_nop 0
	v_addc_co_u32_e32 v169, vcc, 0, v173, vcc
	v_add_co_u32_e32 v202, vcc, s2, v172
	s_mov_b32 s2, 0x1f000
	s_nop 0
	v_addc_co_u32_e32 v203, vcc, 0, v173, vcc
	v_add_co_u32_e32 v170, vcc, s2, v172
	v_readlane_b32 s27, v254, 33
	s_nop 0
	v_addc_co_u32_e32 v171, vcc, 0, v173, vcc
	global_load_dwordx4 v[108:111], v[168:169], off offset:-4096 nt
	global_load_dwordx4 v[112:115], v[170:171], off offset:-4096 nt
	global_load_dwordx4 v[116:119], v[142:143], off offset:-4096 nt
	global_load_dwordx4 v[96:99], v128, s[48:49] offset:1024 nt
	global_load_dwordx4 v[100:103], v[174:175], off offset:1024 nt
	global_load_dwordx4 v[104:107], v[176:177], off offset:1024 nt
	global_load_dwordx4 v[124:127], v[178:179], off offset:1024 nt
	global_load_dwordx4 v[64:67], v[180:181], off offset:1024 nt
	global_load_dwordx4 v[68:71], v[182:183], off offset:1024 nt
	global_load_dwordx4 v[72:75], v[184:185], off offset:1024 nt
	global_load_dwordx4 v[76:79], v[186:187], off offset:1024 nt
	global_load_dwordx4 v[32:35], v[188:189], off offset:1024 nt
	global_load_dwordx4 v[36:39], v[190:191], off offset:1024 nt
	global_load_dwordx4 v[40:43], v[192:193], off offset:1024 nt
	global_load_dwordx4 v[44:47], v[194:195], off offset:1024 nt
	global_load_dwordx4 v[0:3], v[196:197], off offset:1024 nt
	global_load_dwordx4 v[4:7], v[198:199], off offset:1024 nt
	global_load_dwordx4 v[8:11], v[200:201], off offset:1024 nt
	global_load_dwordx4 v[120:123], v128, s[48:49] nt
	global_load_dwordx4 v[12:15], v[202:203], off offset:1024 nt
	v_readlane_b32 s28, v254, 34
	v_readlane_b32 s29, v254, 35
	v_readlane_b32 s30, v254, 36
	v_readlane_b32 s31, v254, 37
	v_lshl_add_u64 v[140:141], s[50:51], 0, v[130:131]
	s_waitcnt vmcnt(1)
; #define LAS __attribute__((address_space(3)))
; __device__ __forceinline__ unsigned pack4_fp8(float a, float b, float c, float d) { int r = 0; r = __builtin_amdgcn_cvt_pk_fp8_f32(a, b, r, false); r = __builtin_amdgcn_cvt_pk_fp8_f32(c, d, r, true); return (unsigned)r; }
; __device__ __forceinline__ void cvt8_to_lds(const f32x4 (&v)[16], LAS unsigned char* tile, int lane, int wv) {
; #pragma unroll
;     for (int i = 0; i < 4; ++i) { u32x4 w; w.x = pack4_fp8(v[0][i] * W8_SCALE, v[1][i] * W8_SCALE, v[2][i] * W8_SCALE, v[3][i] * W8_SCALE); w.y = pack4_fp8(v[4][i] * W8_SCALE, v[5][i] * W8_SCALE, v[6][i] * W8_SCALE, v[7][i] * W8_SCALE);
;         w.z = pack4_fp8(v[8][i] * W8_SCALE, v[9][i] * W8_SCALE, v[10][i] * W8_SCALE, v[11][i] * W8_SCALE); w.w = pack4_fp8(v[12][i] * W8_SCALE, v[13][i] * W8_SCALE, v[14][i] * W8_SCALE, v[15][i] * W8_SCALE);
;         *(LAS u32x4*)(tile + (4 * lane + i) * 128 + ((wv ^ (lane & 7)) << 4)) = w; }
; }
; __device__ __forceinline__ void cvt8_from_lds(const LAS unsigned char* tile, fp8_t* d, int ld_dst, int tid) {
;     const int c = tid & 7;
; #pragma unroll
;     for (int q = 0; q < 4; ++q) { const int r = (tid >> 3) + 64 * q; const u32x4 w = *(const LAS u32x4*)(tile + r * 128 + ((c ^ ((r >> 2) & 7)) << 4));
;         __builtin_nontemporal_store(w, (u32x4*)(d + (size_t)r * ld_dst + 16 * c)); }
; }
; __device__ __forceinline__ void cvt_item_lds(const float* src, int ld_src, fp8_t* dst, int ld_dst, LAS unsigned char* lds, int tid, int wv) {
;     const int lane = tid & 63;
;     const float* s = src + (size_t)(16 * wv) * ld_src + 4 * lane;
;     f32x4 va[16], vb[16];
;     cvt8_load(va, s, ld_src);
; #pragma unroll
;     for (int t = 0; t < 8; t += 2) {
;         cvt8_load(vb, s + (t + 1) * 256, ld_src); __builtin_amdgcn_sched_barrier(0);
;         cvt8_to_lds(va, lds, lane, wv); CVT_LDS_BAR(); __builtin_amdgcn_sched_barrier(0);
;         cvt8_from_lds(lds, dst + (size_t)(t * 256) * ld_dst, ld_dst, tid); __builtin_amdgcn_sched_barrier(0);
;         if (t + 2 < 8) { cvt8_load(va, s + (t + 2) * 256, ld_src); __builtin_amdgcn_sched_barrier(0); }
;         cvt8_to_lds(vb, lds + 32768, lane, wv); CVT_LDS_BAR(); __builtin_amdgcn_sched_barrier(0);
;         cvt8_from_lds(lds + 32768, dst + (size_t)((t + 1) * 256) * ld_dst, ld_dst, tid); __builtin_amdgcn_sched_barrier(0);
;     }
	v_mul_f32_e32 v120, 0x42800000, v120
	v_mul_f32_e32 v116, 0x42800000, v116
	v_mov_b32_e32 v210, v129
	v_cvt_pk_fp8_f32 v210, v120, v116
	v_mul_f32_e32 v16, 0x42800000, v16
	v_mul_f32_e32 v20, 0x42800000, v20
	v_mov_b32_e32 v211, v129
	v_cvt_pk_fp8_f32 v210, v16, v20 op_sel:[0,0,1]
	v_mul_f32_e32 v16, 0x42800000, v24
	v_mul_f32_e32 v20, 0x42800000, v28
	v_cvt_pk_fp8_f32 v211, v16, v20
	v_mul_f32_e32 v16, 0x42800000, v48
	v_mul_f32_e32 v20, 0x42800000, v52
	v_mov_b32_e32 v212, v129
	v_cvt_pk_fp8_f32 v212, v16, v20
	v_mul_f32_e32 v16, 0x42800000, v88
	v_mul_f32_e32 v20, 0x42800000, v92
	v_mov_b32_e32 v213, v129
	v_cvt_pk_fp8_f32 v213, v16, v20
	v_mul_f32_e32 v24, 0x42800000, v56
	v_mul_f32_e32 v28, 0x42800000, v60
	v_cvt_pk_fp8_f32 v211, v24, v28 op_sel:[0,0,1]
	v_mul_f32_e32 v24, 0x42800000, v80
	v_mul_f32_e32 v28, 0x42800000, v84
	v_cvt_pk_fp8_f32 v212, v24, v28 op_sel:[0,0,1]
	v_mul_f32_e32 v24, 0x42800000, v108
	v_mul_f32_e32 v28, 0x42800000, v112
	v_cvt_pk_fp8_f32 v213, v24, v28 op_sel:[0,0,1]
	v_mul_f32_e32 v16, 0x42800000, v121
	v_mul_f32_e32 v20, 0x42800000, v117
	v_mul_f32_e32 v17, 0x42800000, v17
	ds_write_b128 v204, v[210:213]
	v_mov_b32_e32 v210, v129
	v_cvt_pk_fp8_f32 v210, v16, v20
	v_mul_f32_e32 v21, 0x42800000, v21
	v_mul_f32_e32 v16, 0x42800000, v25
	v_mov_b32_e32 v211, v129
	v_cvt_pk_fp8_f32 v210, v17, v21 op_sel:[0,0,1]
	v_mul_f32_e32 v17, 0x42800000, v29
	v_cvt_pk_fp8_f32 v211, v16, v17
	v_mul_f32_e32 v16, 0x42800000, v49
	v_mul_f32_e32 v17, 0x42800000, v53
	v_mov_b32_e32 v212, v129
	v_cvt_pk_fp8_f32 v212, v16, v17
	v_mul_f32_e32 v16, 0x42800000, v89
	v_mul_f32_e32 v17, 0x42800000, v93
	v_mov_b32_e32 v213, v129
	v_cvt_pk_fp8_f32 v213, v16, v17
	v_mul_f32_e32 v20, 0x42800000, v57
	v_mul_f32_e32 v21, 0x42800000, v61
	v_cvt_pk_fp8_f32 v211, v20, v21 op_sel:[0,0,1]
	v_mul_f32_e32 v20, 0x42800000, v81
	v_mul_f32_e32 v21, 0x42800000, v85
	v_cvt_pk_fp8_f32 v212, v20, v21 op_sel:[0,0,1]
	v_mul_f32_e32 v20, 0x42800000, v109
	v_mul_f32_e32 v21, 0x42800000, v113
	v_cvt_pk_fp8_f32 v213, v20, v21 op_sel:[0,0,1]
	v_mul_f32_e32 v16, 0x42800000, v122
	v_mul_f32_e32 v17, 0x42800000, v118
	v_mul_f32_e32 v18, 0x42800000, v18
	ds_write_b128 v204, v[210:213] offset:128
	v_mov_b32_e32 v210, v129
	v_cvt_pk_fp8_f32 v210, v16, v17
	v_mul_f32_e32 v16, 0x42800000, v26
	v_mul_f32_e32 v17, 0x42800000, v30
	v_mov_b32_e32 v211, v129
	v_cvt_pk_fp8_f32 v211, v16, v17
	v_mul_f32_e32 v16, 0x42800000, v50
	v_mul_f32_e32 v17, 0x42800000, v54
	v_mov_b32_e32 v212, v129
	v_cvt_pk_fp8_f32 v212, v16, v17
	v_mul_f32_e32 v16, 0x42800000, v90
	v_mul_f32_e32 v17, 0x42800000, v94
	v_mov_b32_e32 v213, v129
	v_mul_f32_e32 v20, 0x42800000, v22
	v_cvt_pk_fp8_f32 v213, v16, v17
	v_cvt_pk_fp8_f32 v210, v18, v20 op_sel:[0,0,1]
	v_mul_f32_e32 v18, 0x42800000, v58
	v_mul_f32_e32 v20, 0x42800000, v62
	v_cvt_pk_fp8_f32 v211, v18, v20 op_sel:[0,0,1]
	v_mul_f32_e32 v18, 0x42800000, v82
	v_mul_f32_e32 v20, 0x42800000, v86
	v_cvt_pk_fp8_f32 v212, v18, v20 op_sel:[0,0,1]
	v_mul_f32_e32 v18, 0x42800000, v110
	v_mul_f32_e32 v20, 0x42800000, v114
	v_cvt_pk_fp8_f32 v213, v18, v20 op_sel:[0,0,1]
	v_mul_f32_e32 v17, 0x42800000, v123
	v_mul_f32_e32 v18, 0x42800000, v119
	v_mov_b32_e32 v16, v129
	v_cvt_pk_fp8_f32 v16, v17, v18
	v_mul_f32_e32 v19, 0x42800000, v19
	v_mul_f32_e32 v20, 0x42800000, v23
	v_mul_f32_e32 v18, 0x42800000, v27
	v_cvt_pk_fp8_f32 v16, v19, v20 op_sel:[0,0,1]
	v_mul_f32_e32 v19, 0x42800000, v31
	v_mov_b32_e32 v17, v129
	v_cvt_pk_fp8_f32 v17, v18, v19
	v_mul_f32_e32 v20, 0x42800000, v59
	v_mul_f32_e32 v21, 0x42800000, v63
	v_mul_f32_e32 v19, 0x42800000, v51
	v_cvt_pk_fp8_f32 v17, v20, v21 op_sel:[0,0,1]
	v_mul_f32_e32 v20, 0x42800000, v55
	v_mov_b32_e32 v18, v129
	v_cvt_pk_fp8_f32 v18, v19, v20
	v_mul_f32_e32 v21, 0x42800000, v83
	v_mul_f32_e32 v22, 0x42800000, v87
	v_mul_f32_e32 v20, 0x42800000, v91
	v_cvt_pk_fp8_f32 v18, v21, v22 op_sel:[0,0,1]
	v_mul_f32_e32 v21, 0x42800000, v95
	v_mov_b32_e32 v19, v129
	v_cvt_pk_fp8_f32 v19, v20, v21
	v_mul_f32_e32 v22, 0x42800000, v111
	v_mul_f32_e32 v23, 0x42800000, v115
	ds_write_b128 v204, v[210:213] offset:256
	v_cvt_pk_fp8_f32 v19, v22, v23 op_sel:[0,0,1]
	ds_write_b128 v204, v[16:19] offset:384
	s_waitcnt lgkmcnt(0)
	s_barrier
	ds_read_b128 v[16:19], v205
	v_lshl_add_u64 v[20:21], v[140:141], 0, v[132:133]
	s_waitcnt lgkmcnt(0)
	global_store_dwordx4 v[20:21], v[16:19], off nt
	ds_read_b128 v[16:19], v206
	v_lshl_add_u64 v[20:21], v[140:141], 0, v[134:135]
	s_waitcnt lgkmcnt(0)
	global_store_dwordx4 v[20:21], v[16:19], off nt
	ds_read_b128 v[16:19], v207
	v_lshl_add_u64 v[20:21], v[140:141], 0, v[136:137]
	s_waitcnt lgkmcnt(0)
	global_store_dwordx4 v[20:21], v[16:19], off nt
	ds_read_b128 v[16:19], v208
	v_lshl_add_u64 v[20:21], v[140:141], 0, v[138:139]
	s_waitcnt lgkmcnt(0)
; #define LAS __attribute__((address_space(3)))
; __device__ __forceinline__ unsigned pack4_fp8(float a, float b, float c, float d) { int r = 0; r = __builtin_amdgcn_cvt_pk_fp8_f32(a, b, r, false); r = __builtin_amdgcn_cvt_pk_fp8_f32(c, d, r, true); return (unsigned)r; }
; __device__ __forceinline__ void cvt8_to_lds(const f32x4 (&v)[16], LAS unsigned char* tile, int lane, int wv) {
; #pragma unroll
;     for (int i = 0; i < 4; ++i) { u32x4 w; w.x = pack4_fp8(v[0][i] * W8_SCALE, v[1][i] * W8_SCALE, v[2][i] * W8_SCALE, v[3][i] * W8_SCALE); w.y = pack4_fp8(v[4][i] * W8_SCALE, v[5][i] * W8_SCALE, v[6][i] * W8_SCALE, v[7][i] * W8_SCALE);
;         w.z = pack4_fp8(v[8][i] * W8_SCALE, v[9][i] * W8_SCALE, v[10][i] * W8_SCALE, v[11][i] * W8_SCALE); w.w = pack4_fp8(v[12][i] * W8_SCALE, v[13][i] * W8_SCALE, v[14][i] * W8_SCALE, v[15][i] * W8_SCALE);
;         *(LAS u32x4*)(tile + (4 * lane + i) * 128 + ((wv ^ (lane & 7)) << 4)) = w; }
; }
; __device__ __forceinline__ void cvt8_from_lds(const LAS unsigned char* tile, fp8_t* d, int ld_dst, int tid) {
;     const int c = tid & 7;
; #pragma unroll
;     for (int q = 0; q < 4; ++q) { const int r = (tid >> 3) + 64 * q; const u32x4 w = *(const LAS u32x4*)(tile + r * 128 + ((c ^ ((r >> 2) & 7)) << 4));
;         __builtin_nontemporal_store(w, (u32x4*)(d + (size_t)r * ld_dst + 16 * c)); }
; }
; __device__ __forceinline__ void cvt_item_lds(const float* src, int ld_src, fp8_t* dst, int ld_dst, LAS unsigned char* lds, int tid, int wv) {
;     const int lane = tid & 63;
;     const float* s = src + (size_t)(16 * wv) * ld_src + 4 * lane;
;     f32x4 va[16], vb[16];
;     cvt8_load(va, s, ld_src);
; #pragma unroll
;     for (int t = 0; t < 8; t += 2) {
;         cvt8_load(vb, s + (t + 1) * 256, ld_src); __builtin_amdgcn_sched_barrier(0);
;         cvt8_to_lds(va, lds, lane, wv); CVT_LDS_BAR(); __builtin_amdgcn_sched_barrier(0);
;         cvt8_from_lds(lds, dst + (size_t)(t * 256) * ld_dst, ld_dst, tid); __builtin_amdgcn_sched_barrier(0);
;         if (t + 2 < 8) { cvt8_load(va, s + (t + 2) * 256, ld_src); __builtin_amdgcn_sched_barrier(0); }
;         cvt8_to_lds(vb, lds + 32768, lane, wv); CVT_LDS_BAR(); __builtin_amdgcn_sched_barrier(0);
;         cvt8_from_lds(lds + 32768, dst + (size_t)((t + 1) * 256) * ld_dst, ld_dst, tid); __builtin_amdgcn_sched_barrier(0);
;     }
	global_store_dwordx4 v[20:21], v[16:19], off nt
	global_load_dwordx4 v[108:111], v[174:175], off offset:2048 nt
	global_load_dwordx4 v[112:115], v[176:177], off offset:2048 nt
	global_load_dwordx4 v[116:119], v[178:179], off offset:2048 nt
	global_load_dwordx4 v[80:83], v[180:181], off offset:2048 nt
	global_load_dwordx4 v[84:87], v[182:183], off offset:2048 nt
	global_load_dwordx4 v[88:91], v[184:185], off offset:2048 nt
	global_load_dwordx4 v[92:95], v[186:187], off offset:2048 nt
	global_load_dwordx4 v[48:51], v[188:189], off offset:2048 nt
	global_load_dwordx4 v[52:55], v[190:191], off offset:2048 nt
	global_load_dwordx4 v[56:59], v[192:193], off offset:2048 nt
	global_load_dwordx4 v[60:63], v[194:195], off offset:2048 nt
	global_load_dwordx4 v[16:19], v[196:197], off offset:2048 nt
	global_load_dwordx4 v[20:23], v[198:199], off offset:2048 nt
	global_load_dwordx4 v[24:27], v[200:201], off offset:2048 nt
	global_load_dwordx4 v[120:123], v128, s[48:49] offset:2048 nt
	global_load_dwordx4 v[28:31], v[202:203], off offset:2048 nt
	v_mul_f32_e32 v96, 0x42800000, v96
	v_mul_f32_e32 v100, 0x42800000, v100
	v_mov_b32_e32 v210, v129
	v_mul_f32_e32 v64, 0x42800000, v64
	v_mul_f32_e32 v68, 0x42800000, v68
	v_mov_b32_e32 v211, v129
	v_mul_f32_e32 v32, 0x42800000, v32
	v_mul_f32_e32 v36, 0x42800000, v36
	v_mov_b32_e32 v212, v129
	v_mul_f32_e32 v0, 0x42800000, v0
	v_mul_f32_e32 v4, 0x42800000, v4
	v_mov_b32_e32 v213, v129
	v_cvt_pk_fp8_f32 v210, v96, v100
	v_cvt_pk_fp8_f32 v211, v64, v68
	v_cvt_pk_fp8_f32 v212, v32, v36
	v_cvt_pk_fp8_f32 v213, v0, v4
	v_mul_f32_e32 v104, 0x42800000, v104
	v_mul_f32_e32 v124, 0x42800000, v124
	v_mul_f32_e32 v72, 0x42800000, v72
	v_mul_f32_e32 v76, 0x42800000, v76
	v_mul_f32_e32 v40, 0x42800000, v40
	v_mul_f32_e32 v44, 0x42800000, v44
	v_mul_f32_e32 v8, 0x42800000, v8
	s_waitcnt vmcnt(20)
	v_mul_f32_e32 v12, 0x42800000, v12
	v_cvt_pk_fp8_f32 v210, v104, v124 op_sel:[0,0,1]
	v_cvt_pk_fp8_f32 v211, v72, v76 op_sel:[0,0,1]
	v_cvt_pk_fp8_f32 v212, v40, v44 op_sel:[0,0,1]
	v_cvt_pk_fp8_f32 v213, v8, v12 op_sel:[0,0,1]
	v_mul_f32_e32 v0, 0x42800000, v97
	v_mul_f32_e32 v4, 0x42800000, v101
	v_mul_f32_e32 v8, 0x42800000, v105
	ds_write_b128 v204, v[210:213] offset:32768
	v_mov_b32_e32 v210, v129
	v_cvt_pk_fp8_f32 v210, v0, v4
	v_mul_f32_e32 v0, 0x42800000, v65
	v_mul_f32_e32 v4, 0x42800000, v69
	v_mov_b32_e32 v211, v129
	v_cvt_pk_fp8_f32 v211, v0, v4
	v_mul_f32_e32 v0, 0x42800000, v33
	v_mul_f32_e32 v4, 0x42800000, v37
	v_mov_b32_e32 v212, v129
	v_cvt_pk_fp8_f32 v212, v0, v4
	v_mul_f32_e32 v0, 0x42800000, v1
	v_mul_f32_e32 v1, 0x42800000, v5
	v_mov_b32_e32 v213, v129
	v_cvt_pk_fp8_f32 v213, v0, v1
	v_mul_f32_e32 v12, 0x42800000, v125
	v_cvt_pk_fp8_f32 v210, v8, v12 op_sel:[0,0,1]
	v_mul_f32_e32 v8, 0x42800000, v73
	v_mul_f32_e32 v12, 0x42800000, v77
	v_cvt_pk_fp8_f32 v211, v8, v12 op_sel:[0,0,1]
	v_mul_f32_e32 v8, 0x42800000, v41
	v_mul_f32_e32 v12, 0x42800000, v45
	v_mul_f32_e32 v4, 0x42800000, v9
	v_mul_f32_e32 v5, 0x42800000, v13
	v_cvt_pk_fp8_f32 v212, v8, v12 op_sel:[0,0,1]
	v_cvt_pk_fp8_f32 v213, v4, v5 op_sel:[0,0,1]
	v_mul_f32_e32 v0, 0x42800000, v98
	v_mul_f32_e32 v1, 0x42800000, v102
	v_mul_f32_e32 v4, 0x42800000, v106
	ds_write_b128 v204, v[210:213] offset:32896
	v_mov_b32_e32 v210, v129
	v_cvt_pk_fp8_f32 v210, v0, v1
	v_mul_f32_e32 v0, 0x42800000, v66
	v_mul_f32_e32 v1, 0x42800000, v70
	v_mov_b32_e32 v211, v129
	v_cvt_pk_fp8_f32 v211, v0, v1
	v_mul_f32_e32 v0, 0x42800000, v34
	v_mul_f32_e32 v1, 0x42800000, v38
	v_mov_b32_e32 v212, v129
	v_cvt_pk_fp8_f32 v212, v0, v1
	v_mul_f32_e32 v0, 0x42800000, v2
	v_mul_f32_e32 v1, 0x42800000, v6
	v_mov_b32_e32 v213, v129
	v_mul_f32_e32 v5, 0x42800000, v126
	v_cvt_pk_fp8_f32 v213, v0, v1
	v_cvt_pk_fp8_f32 v210, v4, v5 op_sel:[0,0,1]
	v_mul_f32_e32 v4, 0x42800000, v74
	v_mul_f32_e32 v5, 0x42800000, v78
	v_cvt_pk_fp8_f32 v211, v4, v5 op_sel:[0,0,1]
	v_mul_f32_e32 v4, 0x42800000, v42
	v_mul_f32_e32 v5, 0x42800000, v46
	v_cvt_pk_fp8_f32 v212, v4, v5 op_sel:[0,0,1]
	v_mul_f32_e32 v2, 0x42800000, v10
	v_mul_f32_e32 v4, 0x42800000, v14
	v_cvt_pk_fp8_f32 v213, v2, v4 op_sel:[0,0,1]
	v_mul_f32_e32 v1, 0x42800000, v99
	v_mul_f32_e32 v2, 0x42800000, v103
	v_mov_b32_e32 v0, v129
	v_cvt_pk_fp8_f32 v0, v1, v2
	v_mul_f32_e32 v4, 0x42800000, v107
	v_mul_f32_e32 v5, 0x42800000, v127
	v_mul_f32_e32 v2, 0x42800000, v67
	v_cvt_pk_fp8_f32 v0, v4, v5 op_sel:[0,0,1]
	v_mul_f32_e32 v4, 0x42800000, v71
	v_mov_b32_e32 v1, v129
	v_cvt_pk_fp8_f32 v1, v2, v4
	v_mul_f32_e32 v5, 0x42800000, v75
	v_mul_f32_e32 v6, 0x42800000, v79
	v_mul_f32_e32 v4, 0x42800000, v35
	v_cvt_pk_fp8_f32 v1, v5, v6 op_sel:[0,0,1]
	v_mul_f32_e32 v5, 0x42800000, v39
	v_mov_b32_e32 v2, v129
	v_cvt_pk_fp8_f32 v2, v4, v5
	v_mul_f32_e32 v4, 0x42800000, v3
	v_mul_f32_e32 v5, 0x42800000, v7
	v_mov_b32_e32 v3, v129
	v_cvt_pk_fp8_f32 v3, v4, v5
	v_mul_f32_e32 v6, 0x42800000, v43
	v_mul_f32_e32 v8, 0x42800000, v47
	v_cvt_pk_fp8_f32 v2, v6, v8 op_sel:[0,0,1]
	v_mul_f32_e32 v6, 0x42800000, v11
	v_mul_f32_e32 v7, 0x42800000, v15
	v_cvt_pk_fp8_f32 v3, v6, v7 op_sel:[0,0,1]
	ds_write_b128 v204, v[210:213] offset:33024
	ds_write_b128 v204, v[0:3] offset:33152
	s_waitcnt lgkmcnt(0)
	s_barrier
; #define LAS __attribute__((address_space(3)))
; __device__ __forceinline__ unsigned pack4_fp8(float a, float b, float c, float d) { int r = 0; r = __builtin_amdgcn_cvt_pk_fp8_f32(a, b, r, false); r = __builtin_amdgcn_cvt_pk_fp8_f32(c, d, r, true); return (unsigned)r; }
; __device__ __forceinline__ void cvt8_to_lds(const f32x4 (&v)[16], LAS unsigned char* tile, int lane, int wv) {
; #pragma unroll
;     for (int i = 0; i < 4; ++i) { u32x4 w; w.x = pack4_fp8(v[0][i] * W8_SCALE, v[1][i] * W8_SCALE, v[2][i] * W8_SCALE, v[3][i] * W8_SCALE); w.y = pack4_fp8(v[4][i] * W8_SCALE, v[5][i] * W8_SCALE, v[6][i] * W8_SCALE, v[7][i] * W8_SCALE);
;         w.z = pack4_fp8(v[8][i] * W8_SCALE, v[9][i] * W8_SCALE, v[10][i] * W8_SCALE, v[11][i] * W8_SCALE); w.w = pack4_fp8(v[12][i] * W8_SCALE, v[13][i] * W8_SCALE, v[14][i] * W8_SCALE, v[15][i] * W8_SCALE);
;         *(LAS u32x4*)(tile + (4 * lane + i) * 128 + ((wv ^ (lane & 7)) << 4)) = w; }
; }
; __device__ __forceinline__ void cvt8_from_lds(const LAS unsigned char* tile, fp8_t* d, int ld_dst, int tid) {
;     const int c = tid & 7;
; #pragma unroll
;     for (int q = 0; q < 4; ++q) { const int r = (tid >> 3) + 64 * q; const u32x4 w = *(const LAS u32x4*)(tile + r * 128 + ((c ^ ((r >> 2) & 7)) << 4));
;         __builtin_nontemporal_store(w, (u32x4*)(d + (size_t)r * ld_dst + 16 * c)); }
; }
; __device__ __forceinline__ void cvt_item_lds(const float* src, int ld_src, fp8_t* dst, int ld_dst, LAS unsigned char* lds, int tid, int wv) {
;     const int lane = tid & 63;
;     const float* s = src + (size_t)(16 * wv) * ld_src + 4 * lane;
;     f32x4 va[16], vb[16];
;     cvt8_load(va, s, ld_src);
; #pragma unroll
;     for (int t = 0; t < 8; t += 2) {
;         cvt8_load(vb, s + (t + 1) * 256, ld_src); __builtin_amdgcn_sched_barrier(0);
;         cvt8_to_lds(va, lds, lane, wv); CVT_LDS_BAR(); __builtin_amdgcn_sched_barrier(0);
;         cvt8_from_lds(lds, dst + (size_t)(t * 256) * ld_dst, ld_dst, tid); __builtin_amdgcn_sched_barrier(0);
;         if (t + 2 < 8) { cvt8_load(va, s + (t + 2) * 256, ld_src); __builtin_amdgcn_sched_barrier(0); }
;         cvt8_to_lds(vb, lds + 32768, lane, wv); CVT_LDS_BAR(); __builtin_amdgcn_sched_barrier(0);
;         cvt8_from_lds(lds + 32768, dst + (size_t)((t + 1) * 256) * ld_dst, ld_dst, tid); __builtin_amdgcn_sched_barrier(0);
;     }
	ds_read_b128 v[0:3], v205 offset:32768
	v_lshl_add_u64 v[4:5], v[140:141], 0, s[8:9]
	v_lshl_add_u64 v[6:7], v[4:5], 0, v[132:133]
	s_waitcnt lgkmcnt(0)
	global_store_dwordx4 v[6:7], v[0:3], off nt
	ds_read_b128 v[0:3], v206 offset:32768
	v_lshl_add_u64 v[6:7], v[4:5], 0, v[134:135]
	s_waitcnt lgkmcnt(0)
	global_store_dwordx4 v[6:7], v[0:3], off nt
	ds_read_b128 v[0:3], v207 offset:32768
	v_lshl_add_u64 v[6:7], v[4:5], 0, v[136:137]
	v_lshl_add_u64 v[4:5], v[4:5], 0, v[138:139]
	s_waitcnt lgkmcnt(0)
	global_store_dwordx4 v[6:7], v[0:3], off nt
	ds_read_b128 v[0:3], v208 offset:32768
	s_waitcnt lgkmcnt(0)
	global_store_dwordx4 v[4:5], v[0:3], off nt
	global_load_dwordx4 v[96:99], v[174:175], off offset:3072 nt
	global_load_dwordx4 v[100:103], v[176:177], off offset:3072 nt
	global_load_dwordx4 v[104:107], v[178:179], off offset:3072 nt
	global_load_dwordx4 v[64:67], v[180:181], off offset:3072 nt
	global_load_dwordx4 v[68:71], v[182:183], off offset:3072 nt
	global_load_dwordx4 v[72:75], v[184:185], off offset:3072 nt
	global_load_dwordx4 v[76:79], v[186:187], off offset:3072 nt
	global_load_dwordx4 v[32:35], v[188:189], off offset:3072 nt
	global_load_dwordx4 v[36:39], v[190:191], off offset:3072 nt
	global_load_dwordx4 v[40:43], v[192:193], off offset:3072 nt
	global_load_dwordx4 v[44:47], v[194:195], off offset:3072 nt
	global_load_dwordx4 v[0:3], v[196:197], off offset:3072 nt
	global_load_dwordx4 v[4:7], v[198:199], off offset:3072 nt
	global_load_dwordx4 v[8:11], v[200:201], off offset:3072 nt
	global_load_dwordx4 v[124:127], v128, s[48:49] offset:3072 nt
	global_load_dwordx4 v[12:15], v[202:203], off offset:3072 nt
	s_waitcnt vmcnt(21)
	v_mul_f32_e32 v120, 0x42800000, v120
	v_mul_f32_e32 v108, 0x42800000, v108
	v_mov_b32_e32 v174, v129
	v_mul_f32_e32 v80, 0x42800000, v80
	v_mul_f32_e32 v84, 0x42800000, v84
	v_mov_b32_e32 v175, v129
	v_mul_f32_e32 v48, 0x42800000, v48
	v_mul_f32_e32 v52, 0x42800000, v52
	v_mov_b32_e32 v176, v129
	v_mul_f32_e32 v16, 0x42800000, v16
	v_mul_f32_e32 v20, 0x42800000, v20
	v_mov_b32_e32 v177, v129
	v_cvt_pk_fp8_f32 v174, v120, v108
	v_cvt_pk_fp8_f32 v175, v80, v84
	v_cvt_pk_fp8_f32 v176, v48, v52
	v_cvt_pk_fp8_f32 v177, v16, v20
	v_mul_f32_e32 v112, 0x42800000, v112
	v_mul_f32_e32 v116, 0x42800000, v116
	v_mul_f32_e32 v88, 0x42800000, v88
	v_mul_f32_e32 v92, 0x42800000, v92
	v_mul_f32_e32 v56, 0x42800000, v56
	v_mul_f32_e32 v60, 0x42800000, v60
	v_mul_f32_e32 v24, 0x42800000, v24
	s_waitcnt vmcnt(20)
	v_mul_f32_e32 v28, 0x42800000, v28
	v_cvt_pk_fp8_f32 v174, v112, v116 op_sel:[0,0,1]
	v_cvt_pk_fp8_f32 v175, v88, v92 op_sel:[0,0,1]
	v_cvt_pk_fp8_f32 v176, v56, v60 op_sel:[0,0,1]
	v_cvt_pk_fp8_f32 v177, v24, v28 op_sel:[0,0,1]
	v_mul_f32_e32 v16, 0x42800000, v121
	v_mul_f32_e32 v20, 0x42800000, v109
	v_mul_f32_e32 v24, 0x42800000, v113
	ds_write_b128 v204, v[174:177]
	v_mov_b32_e32 v174, v129
	v_cvt_pk_fp8_f32 v174, v16, v20
	v_mul_f32_e32 v16, 0x42800000, v81
	v_mul_f32_e32 v20, 0x42800000, v85
	v_mov_b32_e32 v175, v129
	v_cvt_pk_fp8_f32 v175, v16, v20
	v_mul_f32_e32 v16, 0x42800000, v49
	v_mul_f32_e32 v20, 0x42800000, v53
	v_mov_b32_e32 v176, v129
	v_cvt_pk_fp8_f32 v176, v16, v20
	v_mul_f32_e32 v16, 0x42800000, v17
	v_mul_f32_e32 v17, 0x42800000, v21
	v_mov_b32_e32 v177, v129
	v_cvt_pk_fp8_f32 v177, v16, v17
	v_mul_f32_e32 v28, 0x42800000, v117
	v_cvt_pk_fp8_f32 v174, v24, v28 op_sel:[0,0,1]
	v_mul_f32_e32 v24, 0x42800000, v89
	v_mul_f32_e32 v28, 0x42800000, v93
	v_cvt_pk_fp8_f32 v175, v24, v28 op_sel:[0,0,1]
	v_mul_f32_e32 v24, 0x42800000, v57
	v_mul_f32_e32 v28, 0x42800000, v61
	v_mul_f32_e32 v20, 0x42800000, v25
	v_mul_f32_e32 v21, 0x42800000, v29
	v_cvt_pk_fp8_f32 v176, v24, v28 op_sel:[0,0,1]
	v_cvt_pk_fp8_f32 v177, v20, v21 op_sel:[0,0,1]
	v_mul_f32_e32 v16, 0x42800000, v122
	v_mul_f32_e32 v17, 0x42800000, v110
	v_mul_f32_e32 v20, 0x42800000, v114
	ds_write_b128 v204, v[174:177] offset:128
	v_mov_b32_e32 v174, v129
	v_cvt_pk_fp8_f32 v174, v16, v17
	v_mul_f32_e32 v16, 0x42800000, v82
	v_mul_f32_e32 v17, 0x42800000, v86
	v_mov_b32_e32 v175, v129
	v_cvt_pk_fp8_f32 v175, v16, v17
	v_mul_f32_e32 v16, 0x42800000, v50
	v_mul_f32_e32 v17, 0x42800000, v54
	v_mov_b32_e32 v176, v129
	v_cvt_pk_fp8_f32 v176, v16, v17
	v_mul_f32_e32 v16, 0x42800000, v18
	v_mul_f32_e32 v17, 0x42800000, v22
	v_mov_b32_e32 v177, v129
	v_mul_f32_e32 v21, 0x42800000, v118
	v_cvt_pk_fp8_f32 v177, v16, v17
	v_cvt_pk_fp8_f32 v174, v20, v21 op_sel:[0,0,1]
	v_mul_f32_e32 v20, 0x42800000, v90
	v_mul_f32_e32 v21, 0x42800000, v94
	v_cvt_pk_fp8_f32 v175, v20, v21 op_sel:[0,0,1]
	v_mul_f32_e32 v20, 0x42800000, v58
	v_mul_f32_e32 v21, 0x42800000, v62
	v_cvt_pk_fp8_f32 v176, v20, v21 op_sel:[0,0,1]
	v_mul_f32_e32 v18, 0x42800000, v26
	v_mul_f32_e32 v20, 0x42800000, v30
	v_cvt_pk_fp8_f32 v177, v18, v20 op_sel:[0,0,1]
	v_mul_f32_e32 v17, 0x42800000, v123
	v_mul_f32_e32 v18, 0x42800000, v111
	v_mov_b32_e32 v16, v129
	v_cvt_pk_fp8_f32 v16, v17, v18
	v_mul_f32_e32 v20, 0x42800000, v115
	v_mul_f32_e32 v21, 0x42800000, v119
	v_mul_f32_e32 v18, 0x42800000, v83
	v_cvt_pk_fp8_f32 v16, v20, v21 op_sel:[0,0,1]
	v_mul_f32_e32 v20, 0x42800000, v87
	v_mov_b32_e32 v17, v129
	v_cvt_pk_fp8_f32 v17, v18, v20
	v_mul_f32_e32 v21, 0x42800000, v91
	v_mul_f32_e32 v22, 0x42800000, v95
	v_mul_f32_e32 v20, 0x42800000, v51
	v_cvt_pk_fp8_f32 v17, v21, v22 op_sel:[0,0,1]
	v_mul_f32_e32 v21, 0x42800000, v55
	v_mov_b32_e32 v18, v129
	v_cvt_pk_fp8_f32 v18, v20, v21
	v_mul_f32_e32 v20, 0x42800000, v19
	v_mul_f32_e32 v21, 0x42800000, v23
	v_mov_b32_e32 v19, v129
	v_cvt_pk_fp8_f32 v19, v20, v21
	v_mul_f32_e32 v22, 0x42800000, v59
	v_mul_f32_e32 v24, 0x42800000, v63
	v_cvt_pk_fp8_f32 v18, v22, v24 op_sel:[0,0,1]
	v_mul_f32_e32 v22, 0x42800000, v27
	v_mul_f32_e32 v23, 0x42800000, v31
	v_cvt_pk_fp8_f32 v19, v22, v23 op_sel:[0,0,1]
	ds_write_b128 v204, v[174:177] offset:256
	ds_write_b128 v204, v[16:19] offset:384
	s_waitcnt lgkmcnt(0)
	s_barrier
; #define LAS __attribute__((address_space(3)))
; __device__ __forceinline__ unsigned pack4_fp8(float a, float b, float c, float d) { int r = 0; r = __builtin_amdgcn_cvt_pk_fp8_f32(a, b, r, false); r = __builtin_amdgcn_cvt_pk_fp8_f32(c, d, r, true); return (unsigned)r; }
; __device__ __forceinline__ void cvt8_to_lds(const f32x4 (&v)[16], LAS unsigned char* tile, int lane, int wv) {
; #pragma unroll
;     for (int i = 0; i < 4; ++i) { u32x4 w; w.x = pack4_fp8(v[0][i] * W8_SCALE, v[1][i] * W8_SCALE, v[2][i] * W8_SCALE, v[3][i] * W8_SCALE); w.y = pack4_fp8(v[4][i] * W8_SCALE, v[5][i] * W8_SCALE, v[6][i] * W8_SCALE, v[7][i] * W8_SCALE);
;         w.z = pack4_fp8(v[8][i] * W8_SCALE, v[9][i] * W8_SCALE, v[10][i] * W8_SCALE, v[11][i] * W8_SCALE); w.w = pack4_fp8(v[12][i] * W8_SCALE, v[13][i] * W8_SCALE, v[14][i] * W8_SCALE, v[15][i] * W8_SCALE);
;         *(LAS u32x4*)(tile + (4 * lane + i) * 128 + ((wv ^ (lane & 7)) << 4)) = w; }
; }
; __device__ __forceinline__ void cvt8_from_lds(const LAS unsigned char* tile, fp8_t* d, int ld_dst, int tid) {
;     const int c = tid & 7;
; #pragma unroll
;     for (int q = 0; q < 4; ++q) { const int r = (tid >> 3) + 64 * q; const u32x4 w = *(const LAS u32x4*)(tile + r * 128 + ((c ^ ((r >> 2) & 7)) << 4));
;         __builtin_nontemporal_store(w, (u32x4*)(d + (size_t)r * ld_dst + 16 * c)); }
; }
; __device__ __forceinline__ void cvt_item_lds(const float* src, int ld_src, fp8_t* dst, int ld_dst, LAS unsigned char* lds, int tid, int wv) {
;     const int lane = tid & 63;
;     const float* s = src + (size_t)(16 * wv) * ld_src + 4 * lane;
;     f32x4 va[16], vb[16];
;     cvt8_load(va, s, ld_src);
; #pragma unroll
;     for (int t = 0; t < 8; t += 2) {
;         cvt8_load(vb, s + (t + 1) * 256, ld_src); __builtin_amdgcn_sched_barrier(0);
;         cvt8_to_lds(va, lds, lane, wv); CVT_LDS_BAR(); __builtin_amdgcn_sched_barrier(0);
;         cvt8_from_lds(lds, dst + (size_t)(t * 256) * ld_dst, ld_dst, tid); __builtin_amdgcn_sched_barrier(0);
;         if (t + 2 < 8) { cvt8_load(va, s + (t + 2) * 256, ld_src); __builtin_amdgcn_sched_barrier(0); }
;         cvt8_to_lds(vb, lds + 32768, lane, wv); CVT_LDS_BAR(); __builtin_amdgcn_sched_barrier(0);
;         cvt8_from_lds(lds + 32768, dst + (size_t)((t + 1) * 256) * ld_dst, ld_dst, tid); __builtin_amdgcn_sched_barrier(0);
;     }
	ds_read_b128 v[16:19], v205
	v_lshl_add_u64 v[20:21], v[140:141], 0, s[10:11]
	v_lshl_add_u64 v[22:23], v[20:21], 0, v[132:133]
	s_waitcnt lgkmcnt(0)
	global_store_dwordx4 v[22:23], v[16:19], off nt
	ds_read_b128 v[16:19], v206
	v_lshl_add_u64 v[22:23], v[20:21], 0, v[134:135]
	s_waitcnt lgkmcnt(0)
	global_store_dwordx4 v[22:23], v[16:19], off nt
	ds_read_b128 v[16:19], v207
	v_lshl_add_u64 v[22:23], v[20:21], 0, v[136:137]
	v_lshl_add_u64 v[20:21], v[20:21], 0, v[138:139]
	s_waitcnt lgkmcnt(0)
	global_store_dwordx4 v[22:23], v[16:19], off nt
	ds_read_b128 v[16:19], v208
	s_waitcnt lgkmcnt(0)
	global_store_dwordx4 v[20:21], v[16:19], off nt
	v_add_co_u32_e32 v172, vcc, s66, v172
	s_nop 1
	v_addc_co_u32_e32 v173, vcc, 0, v173, vcc
	global_load_dwordx4 v[108:111], v[172:173], off nt
	global_load_dwordx4 v[112:115], v[142:143], off nt
	global_load_dwordx4 v[116:119], v[144:145], off nt
	global_load_dwordx4 v[120:123], v[146:147], off nt
	global_load_dwordx4 v[80:83], v[148:149], off nt
	global_load_dwordx4 v[84:87], v[150:151], off nt
	global_load_dwordx4 v[88:91], v[152:153], off nt
	global_load_dwordx4 v[92:95], v[154:155], off nt
	global_load_dwordx4 v[48:51], v[156:157], off nt
	global_load_dwordx4 v[52:55], v[158:159], off nt
	global_load_dwordx4 v[56:59], v[160:161], off nt
	global_load_dwordx4 v[60:63], v[162:163], off nt
	global_load_dwordx4 v[16:19], v[164:165], off nt
	global_load_dwordx4 v[20:23], v[166:167], off nt
	global_load_dwordx4 v[24:27], v[168:169], off nt
	global_load_dwordx4 v[28:31], v[170:171], off nt
	s_waitcnt vmcnt(21)
	v_mul_f32_e32 v124, 0x42800000, v124
	v_mul_f32_e32 v96, 0x42800000, v96
	v_mov_b32_e32 v174, v129
	v_mul_f32_e32 v64, 0x42800000, v64
	v_mul_f32_e32 v68, 0x42800000, v68
	v_mov_b32_e32 v175, v129
	v_mul_f32_e32 v32, 0x42800000, v32
	v_mul_f32_e32 v36, 0x42800000, v36
	v_mov_b32_e32 v176, v129
	v_mul_f32_e32 v0, 0x42800000, v0
	v_mul_f32_e32 v4, 0x42800000, v4
	v_mov_b32_e32 v177, v129
	v_cvt_pk_fp8_f32 v174, v124, v96
	v_cvt_pk_fp8_f32 v175, v64, v68
	v_cvt_pk_fp8_f32 v176, v32, v36
	v_cvt_pk_fp8_f32 v177, v0, v4
	v_mul_f32_e32 v100, 0x42800000, v100
	v_mul_f32_e32 v104, 0x42800000, v104
	v_mul_f32_e32 v72, 0x42800000, v72
	v_mul_f32_e32 v76, 0x42800000, v76
	v_mul_f32_e32 v40, 0x42800000, v40
	v_mul_f32_e32 v44, 0x42800000, v44
	v_mul_f32_e32 v8, 0x42800000, v8
	s_waitcnt vmcnt(20)
	v_mul_f32_e32 v12, 0x42800000, v12
	v_cvt_pk_fp8_f32 v174, v100, v104 op_sel:[0,0,1]
	v_cvt_pk_fp8_f32 v175, v72, v76 op_sel:[0,0,1]
	v_cvt_pk_fp8_f32 v176, v40, v44 op_sel:[0,0,1]
	v_cvt_pk_fp8_f32 v177, v8, v12 op_sel:[0,0,1]
	v_mul_f32_e32 v0, 0x42800000, v125
	v_mul_f32_e32 v4, 0x42800000, v97
	v_mul_f32_e32 v8, 0x42800000, v101
	ds_write_b128 v204, v[174:177] offset:32768
	v_mov_b32_e32 v174, v129
	v_cvt_pk_fp8_f32 v174, v0, v4
	v_mul_f32_e32 v0, 0x42800000, v65
	v_mul_f32_e32 v4, 0x42800000, v69
	v_mov_b32_e32 v175, v129
	v_cvt_pk_fp8_f32 v175, v0, v4
	v_mul_f32_e32 v0, 0x42800000, v33
	v_mul_f32_e32 v4, 0x42800000, v37
	v_mov_b32_e32 v176, v129
	v_cvt_pk_fp8_f32 v176, v0, v4
	v_mul_f32_e32 v0, 0x42800000, v1
	v_mul_f32_e32 v1, 0x42800000, v5
	v_mov_b32_e32 v177, v129
	v_cvt_pk_fp8_f32 v177, v0, v1
	v_mul_f32_e32 v12, 0x42800000, v105
	v_cvt_pk_fp8_f32 v174, v8, v12 op_sel:[0,0,1]
	v_mul_f32_e32 v8, 0x42800000, v73
	v_mul_f32_e32 v12, 0x42800000, v77
	v_cvt_pk_fp8_f32 v175, v8, v12 op_sel:[0,0,1]
	v_mul_f32_e32 v8, 0x42800000, v41
	v_mul_f32_e32 v12, 0x42800000, v45
	v_mul_f32_e32 v4, 0x42800000, v9
	v_mul_f32_e32 v5, 0x42800000, v13
	v_cvt_pk_fp8_f32 v176, v8, v12 op_sel:[0,0,1]
	v_cvt_pk_fp8_f32 v177, v4, v5 op_sel:[0,0,1]
	v_mul_f32_e32 v0, 0x42800000, v126
	v_mul_f32_e32 v1, 0x42800000, v98
	v_mul_f32_e32 v4, 0x42800000, v102
	ds_write_b128 v204, v[174:177] offset:32896
	v_mov_b32_e32 v174, v129
	v_cvt_pk_fp8_f32 v174, v0, v1
	v_mul_f32_e32 v0, 0x42800000, v66
	v_mul_f32_e32 v1, 0x42800000, v70
	v_mov_b32_e32 v175, v129
	v_cvt_pk_fp8_f32 v175, v0, v1
	v_mul_f32_e32 v0, 0x42800000, v34
	v_mul_f32_e32 v1, 0x42800000, v38
	v_mov_b32_e32 v176, v129
	v_cvt_pk_fp8_f32 v176, v0, v1
	v_mul_f32_e32 v0, 0x42800000, v2
	v_mul_f32_e32 v1, 0x42800000, v6
	v_mov_b32_e32 v177, v129
	v_mul_f32_e32 v5, 0x42800000, v106
	v_cvt_pk_fp8_f32 v177, v0, v1
	v_cvt_pk_fp8_f32 v174, v4, v5 op_sel:[0,0,1]
	v_mul_f32_e32 v4, 0x42800000, v74
	v_mul_f32_e32 v5, 0x42800000, v78
	v_cvt_pk_fp8_f32 v175, v4, v5 op_sel:[0,0,1]
	v_mul_f32_e32 v4, 0x42800000, v42
	v_mul_f32_e32 v5, 0x42800000, v46
	v_cvt_pk_fp8_f32 v176, v4, v5 op_sel:[0,0,1]
	v_mul_f32_e32 v2, 0x42800000, v10
	v_mul_f32_e32 v4, 0x42800000, v14
	v_cvt_pk_fp8_f32 v177, v2, v4 op_sel:[0,0,1]
	v_mul_f32_e32 v1, 0x42800000, v127
	v_mul_f32_e32 v2, 0x42800000, v99
	v_mov_b32_e32 v0, v129
	v_cvt_pk_fp8_f32 v0, v1, v2
	v_mul_f32_e32 v4, 0x42800000, v103
	v_mul_f32_e32 v5, 0x42800000, v107
	v_mul_f32_e32 v2, 0x42800000, v67
	v_cvt_pk_fp8_f32 v0, v4, v5 op_sel:[0,0,1]
	v_mul_f32_e32 v4, 0x42800000, v71
	v_mov_b32_e32 v1, v129
	v_cvt_pk_fp8_f32 v1, v2, v4
	v_mul_f32_e32 v5, 0x42800000, v75
	v_mul_f32_e32 v6, 0x42800000, v79
	v_mul_f32_e32 v4, 0x42800000, v35
	v_cvt_pk_fp8_f32 v1, v5, v6 op_sel:[0,0,1]
	v_mul_f32_e32 v5, 0x42800000, v39
	v_mov_b32_e32 v2, v129
	v_cvt_pk_fp8_f32 v2, v4, v5
	v_mul_f32_e32 v4, 0x42800000, v3
	v_mul_f32_e32 v5, 0x42800000, v7
	v_mov_b32_e32 v3, v129
	v_cvt_pk_fp8_f32 v3, v4, v5
	v_mul_f32_e32 v6, 0x42800000, v43
	v_mul_f32_e32 v8, 0x42800000, v47
	v_cvt_pk_fp8_f32 v2, v6, v8 op_sel:[0,0,1]
	v_mul_f32_e32 v6, 0x42800000, v11
	v_mul_f32_e32 v7, 0x42800000, v15
	v_cvt_pk_fp8_f32 v3, v6, v7 op_sel:[0,0,1]
	ds_write_b128 v204, v[174:177] offset:33024
	ds_write_b128 v204, v[0:3] offset:33152
	s_waitcnt lgkmcnt(0)
	s_barrier
; #define LAS __attribute__((address_space(3)))
; __device__ __forceinline__ unsigned pack4_fp8(float a, float b, float c, float d) { int r = 0; r = __builtin_amdgcn_cvt_pk_fp8_f32(a, b, r, false); r = __builtin_amdgcn_cvt_pk_fp8_f32(c, d, r, true); return (unsigned)r; }
; __device__ __forceinline__ void cvt8_to_lds(const f32x4 (&v)[16], LAS unsigned char* tile, int lane, int wv) {
; #pragma unroll
;     for (int i = 0; i < 4; ++i) { u32x4 w; w.x = pack4_fp8(v[0][i] * W8_SCALE, v[1][i] * W8_SCALE, v[2][i] * W8_SCALE, v[3][i] * W8_SCALE); w.y = pack4_fp8(v[4][i] * W8_SCALE, v[5][i] * W8_SCALE, v[6][i] * W8_SCALE, v[7][i] * W8_SCALE);
;         w.z = pack4_fp8(v[8][i] * W8_SCALE, v[9][i] * W8_SCALE, v[10][i] * W8_SCALE, v[11][i] * W8_SCALE); w.w = pack4_fp8(v[12][i] * W8_SCALE, v[13][i] * W8_SCALE, v[14][i] * W8_SCALE, v[15][i] * W8_SCALE);
;         *(LAS u32x4*)(tile + (4 * lane + i) * 128 + ((wv ^ (lane & 7)) << 4)) = w; }
; }
; __device__ __forceinline__ void cvt8_from_lds(const LAS unsigned char* tile, fp8_t* d, int ld_dst, int tid) {
;     const int c = tid & 7;
; #pragma unroll
;     for (int q = 0; q < 4; ++q) { const int r = (tid >> 3) + 64 * q; const u32x4 w = *(const LAS u32x4*)(tile + r * 128 + ((c ^ ((r >> 2) & 7)) << 4));
;         __builtin_nontemporal_store(w, (u32x4*)(d + (size_t)r * ld_dst + 16 * c)); }
; }
; __device__ __forceinline__ void cvt_item_lds(const float* src, int ld_src, fp8_t* dst, int ld_dst, LAS unsigned char* lds, int tid, int wv) {
;     const int lane = tid & 63;
;     const float* s = src + (size_t)(16 * wv) * ld_src + 4 * lane;
;     f32x4 va[16], vb[16];
;     cvt8_load(va, s, ld_src);
; #pragma unroll
;     for (int t = 0; t < 8; t += 2) {
;         cvt8_load(vb, s + (t + 1) * 256, ld_src); __builtin_amdgcn_sched_barrier(0);
;         cvt8_to_lds(va, lds, lane, wv); CVT_LDS_BAR(); __builtin_amdgcn_sched_barrier(0);
;         cvt8_from_lds(lds, dst + (size_t)(t * 256) * ld_dst, ld_dst, tid); __builtin_amdgcn_sched_barrier(0);
;         if (t + 2 < 8) { cvt8_load(va, s + (t + 2) * 256, ld_src); __builtin_amdgcn_sched_barrier(0); }
;         cvt8_to_lds(vb, lds + 32768, lane, wv); CVT_LDS_BAR(); __builtin_amdgcn_sched_barrier(0);
;         cvt8_from_lds(lds + 32768, dst + (size_t)((t + 1) * 256) * ld_dst, ld_dst, tid); __builtin_amdgcn_sched_barrier(0);
;     }
	ds_read_b128 v[0:3], v205 offset:32768
	v_lshl_add_u64 v[4:5], v[140:141], 0, s[38:39]
	v_lshl_add_u64 v[6:7], v[4:5], 0, v[132:133]
	s_waitcnt lgkmcnt(0)
	global_store_dwordx4 v[6:7], v[0:3], off nt
	ds_read_b128 v[0:3], v206 offset:32768
	v_lshl_add_u64 v[6:7], v[4:5], 0, v[134:135]
	s_waitcnt lgkmcnt(0)
	global_store_dwordx4 v[6:7], v[0:3], off nt
	ds_read_b128 v[0:3], v207 offset:32768
	v_lshl_add_u64 v[6:7], v[4:5], 0, v[136:137]
	v_lshl_add_u64 v[4:5], v[4:5], 0, v[138:139]
	s_waitcnt lgkmcnt(0)
	global_store_dwordx4 v[6:7], v[0:3], off nt
	ds_read_b128 v[0:3], v208 offset:32768
	s_waitcnt lgkmcnt(0)
	global_store_dwordx4 v[4:5], v[0:3], off nt
	global_load_dwordx4 v[96:99], v[172:173], off offset:1024 nt
	global_load_dwordx4 v[100:103], v[142:143], off offset:1024 nt
	global_load_dwordx4 v[104:107], v[144:145], off offset:1024 nt
	global_load_dwordx4 v[124:127], v[146:147], off offset:1024 nt
	global_load_dwordx4 v[64:67], v[148:149], off offset:1024 nt
	global_load_dwordx4 v[68:71], v[150:151], off offset:1024 nt
	global_load_dwordx4 v[72:75], v[152:153], off offset:1024 nt
	global_load_dwordx4 v[76:79], v[154:155], off offset:1024 nt
	global_load_dwordx4 v[32:35], v[156:157], off offset:1024 nt
	global_load_dwordx4 v[36:39], v[158:159], off offset:1024 nt
	global_load_dwordx4 v[40:43], v[160:161], off offset:1024 nt
	global_load_dwordx4 v[44:47], v[162:163], off offset:1024 nt
	global_load_dwordx4 v[0:3], v[164:165], off offset:1024 nt
	global_load_dwordx4 v[4:7], v[166:167], off offset:1024 nt
	global_load_dwordx4 v[8:11], v[168:169], off offset:1024 nt
	global_load_dwordx4 v[12:15], v[170:171], off offset:1024 nt
	s_waitcnt vmcnt(35)
	v_mul_f32_e32 v108, 0x42800000, v108
	s_waitcnt vmcnt(34)
	v_mul_f32_e32 v112, 0x42800000, v112
	v_mov_b32_e32 v174, v129
	s_waitcnt vmcnt(31)
	v_mul_f32_e32 v80, 0x42800000, v80
	s_waitcnt vmcnt(30)
	v_mul_f32_e32 v84, 0x42800000, v84
	v_mov_b32_e32 v175, v129
	s_waitcnt vmcnt(27)
	v_mul_f32_e32 v48, 0x42800000, v48
	s_waitcnt vmcnt(26)
	v_mul_f32_e32 v52, 0x42800000, v52
	v_mov_b32_e32 v176, v129
	s_waitcnt vmcnt(23)
	v_mul_f32_e32 v16, 0x42800000, v16
	s_waitcnt vmcnt(22)
	v_mul_f32_e32 v20, 0x42800000, v20
	v_mov_b32_e32 v177, v129
	v_cvt_pk_fp8_f32 v174, v108, v112
	v_cvt_pk_fp8_f32 v175, v80, v84
	v_cvt_pk_fp8_f32 v176, v48, v52
	v_cvt_pk_fp8_f32 v177, v16, v20
	v_mul_f32_e32 v116, 0x42800000, v116
	v_mul_f32_e32 v120, 0x42800000, v120
	v_mul_f32_e32 v88, 0x42800000, v88
	v_mul_f32_e32 v92, 0x42800000, v92
	v_mul_f32_e32 v56, 0x42800000, v56
	v_mul_f32_e32 v60, 0x42800000, v60
	s_waitcnt vmcnt(21)
	v_mul_f32_e32 v24, 0x42800000, v24
	s_waitcnt vmcnt(20)
	v_mul_f32_e32 v28, 0x42800000, v28
	v_cvt_pk_fp8_f32 v174, v116, v120 op_sel:[0,0,1]
	v_cvt_pk_fp8_f32 v175, v88, v92 op_sel:[0,0,1]
	v_cvt_pk_fp8_f32 v176, v56, v60 op_sel:[0,0,1]
	v_cvt_pk_fp8_f32 v177, v24, v28 op_sel:[0,0,1]
	v_mul_f32_e32 v16, 0x42800000, v109
	v_mul_f32_e32 v20, 0x42800000, v113
	v_mul_f32_e32 v24, 0x42800000, v117
	ds_write_b128 v204, v[174:177]
	v_mov_b32_e32 v174, v129
	v_cvt_pk_fp8_f32 v174, v16, v20
	v_mul_f32_e32 v16, 0x42800000, v81
	v_mul_f32_e32 v20, 0x42800000, v85
	v_mov_b32_e32 v175, v129
	v_cvt_pk_fp8_f32 v175, v16, v20
	v_mul_f32_e32 v16, 0x42800000, v49
	v_mul_f32_e32 v20, 0x42800000, v53
	v_mov_b32_e32 v176, v129
	v_cvt_pk_fp8_f32 v176, v16, v20
	v_mul_f32_e32 v16, 0x42800000, v17
	v_mul_f32_e32 v17, 0x42800000, v21
	v_mov_b32_e32 v177, v129
	v_cvt_pk_fp8_f32 v177, v16, v17
	v_mul_f32_e32 v28, 0x42800000, v121
	v_cvt_pk_fp8_f32 v174, v24, v28 op_sel:[0,0,1]
	v_mul_f32_e32 v24, 0x42800000, v89
	v_mul_f32_e32 v28, 0x42800000, v93
	v_cvt_pk_fp8_f32 v175, v24, v28 op_sel:[0,0,1]
	v_mul_f32_e32 v24, 0x42800000, v57
	v_mul_f32_e32 v28, 0x42800000, v61
	v_mul_f32_e32 v20, 0x42800000, v25
	v_mul_f32_e32 v21, 0x42800000, v29
	v_cvt_pk_fp8_f32 v176, v24, v28 op_sel:[0,0,1]
	v_cvt_pk_fp8_f32 v177, v20, v21 op_sel:[0,0,1]
	v_mul_f32_e32 v16, 0x42800000, v110
	v_mul_f32_e32 v17, 0x42800000, v114
	v_mul_f32_e32 v20, 0x42800000, v118
	ds_write_b128 v204, v[174:177] offset:128
	v_mov_b32_e32 v174, v129
	v_cvt_pk_fp8_f32 v174, v16, v17
	v_mul_f32_e32 v16, 0x42800000, v82
	v_mul_f32_e32 v17, 0x42800000, v86
	v_mov_b32_e32 v175, v129
	v_cvt_pk_fp8_f32 v175, v16, v17
	v_mul_f32_e32 v16, 0x42800000, v50
	v_mul_f32_e32 v17, 0x42800000, v54
	v_mov_b32_e32 v176, v129
	v_cvt_pk_fp8_f32 v176, v16, v17
	v_mul_f32_e32 v16, 0x42800000, v18
	v_mul_f32_e32 v17, 0x42800000, v22
	v_mov_b32_e32 v177, v129
	v_mul_f32_e32 v21, 0x42800000, v122
	v_cvt_pk_fp8_f32 v177, v16, v17
	v_cvt_pk_fp8_f32 v174, v20, v21 op_sel:[0,0,1]
	v_mul_f32_e32 v20, 0x42800000, v90
	v_mul_f32_e32 v21, 0x42800000, v94
	v_cvt_pk_fp8_f32 v175, v20, v21 op_sel:[0,0,1]
	v_mul_f32_e32 v20, 0x42800000, v58
	v_mul_f32_e32 v21, 0x42800000, v62
	v_cvt_pk_fp8_f32 v176, v20, v21 op_sel:[0,0,1]
	v_mul_f32_e32 v18, 0x42800000, v26
	v_mul_f32_e32 v20, 0x42800000, v30
	v_cvt_pk_fp8_f32 v177, v18, v20 op_sel:[0,0,1]
	v_mul_f32_e32 v17, 0x42800000, v111
	v_mul_f32_e32 v18, 0x42800000, v115
	v_mov_b32_e32 v16, v129
	v_cvt_pk_fp8_f32 v16, v17, v18
	v_mul_f32_e32 v20, 0x42800000, v119
	v_mul_f32_e32 v21, 0x42800000, v123
	v_mul_f32_e32 v18, 0x42800000, v83
	v_cvt_pk_fp8_f32 v16, v20, v21 op_sel:[0,0,1]
	v_mul_f32_e32 v20, 0x42800000, v87
	v_mov_b32_e32 v17, v129
	v_cvt_pk_fp8_f32 v17, v18, v20
	v_mul_f32_e32 v21, 0x42800000, v91
	v_mul_f32_e32 v22, 0x42800000, v95
	v_mul_f32_e32 v20, 0x42800000, v51
	v_cvt_pk_fp8_f32 v17, v21, v22 op_sel:[0,0,1]
	v_mul_f32_e32 v21, 0x42800000, v55
	v_mov_b32_e32 v18, v129
	v_cvt_pk_fp8_f32 v18, v20, v21
	v_mul_f32_e32 v20, 0x42800000, v19
	v_mul_f32_e32 v21, 0x42800000, v23
	v_mov_b32_e32 v19, v129
	v_cvt_pk_fp8_f32 v19, v20, v21
	v_mul_f32_e32 v22, 0x42800000, v59
	v_mul_f32_e32 v24, 0x42800000, v63
	v_cvt_pk_fp8_f32 v18, v22, v24 op_sel:[0,0,1]
	v_mul_f32_e32 v22, 0x42800000, v27
	v_mul_f32_e32 v23, 0x42800000, v31
	v_cvt_pk_fp8_f32 v19, v22, v23 op_sel:[0,0,1]
	ds_write_b128 v204, v[174:177] offset:256
	ds_write_b128 v204, v[16:19] offset:384
	s_waitcnt lgkmcnt(0)
	s_barrier
; #define LAS __attribute__((address_space(3)))
; __device__ __forceinline__ unsigned pack4_fp8(float a, float b, float c, float d) { int r = 0; r = __builtin_amdgcn_cvt_pk_fp8_f32(a, b, r, false); r = __builtin_amdgcn_cvt_pk_fp8_f32(c, d, r, true); return (unsigned)r; }
; __device__ __forceinline__ void cvt8_to_lds(const f32x4 (&v)[16], LAS unsigned char* tile, int lane, int wv) {
; #pragma unroll
;     for (int i = 0; i < 4; ++i) { u32x4 w; w.x = pack4_fp8(v[0][i] * W8_SCALE, v[1][i] * W8_SCALE, v[2][i] * W8_SCALE, v[3][i] * W8_SCALE); w.y = pack4_fp8(v[4][i] * W8_SCALE, v[5][i] * W8_SCALE, v[6][i] * W8_SCALE, v[7][i] * W8_SCALE);
;         w.z = pack4_fp8(v[8][i] * W8_SCALE, v[9][i] * W8_SCALE, v[10][i] * W8_SCALE, v[11][i] * W8_SCALE); w.w = pack4_fp8(v[12][i] * W8_SCALE, v[13][i] * W8_SCALE, v[14][i] * W8_SCALE, v[15][i] * W8_SCALE);
;         *(LAS u32x4*)(tile + (4 * lane + i) * 128 + ((wv ^ (lane & 7)) << 4)) = w; }
; }
; __device__ __forceinline__ void cvt8_from_lds(const LAS unsigned char* tile, fp8_t* d, int ld_dst, int tid) {
;     const int c = tid & 7;
; #pragma unroll
;     for (int q = 0; q < 4; ++q) { const int r = (tid >> 3) + 64 * q; const u32x4 w = *(const LAS u32x4*)(tile + r * 128 + ((c ^ ((r >> 2) & 7)) << 4));
;         __builtin_nontemporal_store(w, (u32x4*)(d + (size_t)r * ld_dst + 16 * c)); }
; }
; __device__ __forceinline__ void cvt_item_lds(const float* src, int ld_src, fp8_t* dst, int ld_dst, LAS unsigned char* lds, int tid, int wv) {
;     const int lane = tid & 63;
;     const float* s = src + (size_t)(16 * wv) * ld_src + 4 * lane;
;     f32x4 va[16], vb[16];
;     cvt8_load(va, s, ld_src);
; #pragma unroll
;     for (int t = 0; t < 8; t += 2) {
;         cvt8_load(vb, s + (t + 1) * 256, ld_src); __builtin_amdgcn_sched_barrier(0);
;         cvt8_to_lds(va, lds, lane, wv); CVT_LDS_BAR(); __builtin_amdgcn_sched_barrier(0);
;         cvt8_from_lds(lds, dst + (size_t)(t * 256) * ld_dst, ld_dst, tid); __builtin_amdgcn_sched_barrier(0);
;         if (t + 2 < 8) { cvt8_load(va, s + (t + 2) * 256, ld_src); __builtin_amdgcn_sched_barrier(0); }
;         cvt8_to_lds(vb, lds + 32768, lane, wv); CVT_LDS_BAR(); __builtin_amdgcn_sched_barrier(0);
;         cvt8_from_lds(lds + 32768, dst + (size_t)((t + 1) * 256) * ld_dst, ld_dst, tid); __builtin_amdgcn_sched_barrier(0);
;     }
	ds_read_b128 v[16:19], v205
	v_lshl_add_u64 v[20:21], v[140:141], 0, s[40:41]
	v_lshl_add_u64 v[22:23], v[20:21], 0, v[132:133]
	s_waitcnt lgkmcnt(0)
	global_store_dwordx4 v[22:23], v[16:19], off nt
	ds_read_b128 v[16:19], v206
	v_lshl_add_u64 v[22:23], v[20:21], 0, v[134:135]
	s_waitcnt lgkmcnt(0)
	global_store_dwordx4 v[22:23], v[16:19], off nt
	ds_read_b128 v[16:19], v207
	v_lshl_add_u64 v[22:23], v[20:21], 0, v[136:137]
	v_lshl_add_u64 v[20:21], v[20:21], 0, v[138:139]
	s_waitcnt lgkmcnt(0)
	global_store_dwordx4 v[22:23], v[16:19], off nt
	ds_read_b128 v[16:19], v208
	s_waitcnt lgkmcnt(0)
	global_store_dwordx4 v[20:21], v[16:19], off nt
	global_load_dwordx4 v[108:111], v[172:173], off offset:2048 nt
	global_load_dwordx4 v[112:115], v[142:143], off offset:2048 nt
	global_load_dwordx4 v[116:119], v[144:145], off offset:2048 nt
	global_load_dwordx4 v[120:123], v[146:147], off offset:2048 nt
	global_load_dwordx4 v[80:83], v[148:149], off offset:2048 nt
	global_load_dwordx4 v[84:87], v[150:151], off offset:2048 nt
	global_load_dwordx4 v[88:91], v[152:153], off offset:2048 nt
	global_load_dwordx4 v[92:95], v[154:155], off offset:2048 nt
	global_load_dwordx4 v[48:51], v[156:157], off offset:2048 nt
	global_load_dwordx4 v[52:55], v[158:159], off offset:2048 nt
	global_load_dwordx4 v[56:59], v[160:161], off offset:2048 nt
	global_load_dwordx4 v[60:63], v[162:163], off offset:2048 nt
	global_load_dwordx4 v[16:19], v[164:165], off offset:2048 nt
	global_load_dwordx4 v[20:23], v[166:167], off offset:2048 nt
	global_load_dwordx4 v[24:27], v[168:169], off offset:2048 nt
	global_load_dwordx4 v[28:31], v[170:171], off offset:2048 nt
	s_waitcnt vmcnt(35)
	v_mul_f32_e32 v96, 0x42800000, v96
	s_waitcnt vmcnt(34)
	v_mul_f32_e32 v100, 0x42800000, v100
	v_mov_b32_e32 v174, v129
	s_waitcnt vmcnt(31)
	v_mul_f32_e32 v64, 0x42800000, v64
	s_waitcnt vmcnt(30)
	v_mul_f32_e32 v68, 0x42800000, v68
	v_mov_b32_e32 v175, v129
	s_waitcnt vmcnt(27)
	v_mul_f32_e32 v32, 0x42800000, v32
	s_waitcnt vmcnt(26)
	v_mul_f32_e32 v36, 0x42800000, v36
	v_mov_b32_e32 v176, v129
	s_waitcnt vmcnt(23)
	v_mul_f32_e32 v0, 0x42800000, v0
	s_waitcnt vmcnt(22)
	v_mul_f32_e32 v4, 0x42800000, v4
	v_mov_b32_e32 v177, v129
	v_cvt_pk_fp8_f32 v174, v96, v100
	v_cvt_pk_fp8_f32 v175, v64, v68
	v_cvt_pk_fp8_f32 v176, v32, v36
	v_cvt_pk_fp8_f32 v177, v0, v4
	v_mul_f32_e32 v104, 0x42800000, v104
	v_mul_f32_e32 v124, 0x42800000, v124
	v_mul_f32_e32 v72, 0x42800000, v72
	v_mul_f32_e32 v76, 0x42800000, v76
	v_mul_f32_e32 v40, 0x42800000, v40
	v_mul_f32_e32 v44, 0x42800000, v44
	s_waitcnt vmcnt(21)
	v_mul_f32_e32 v8, 0x42800000, v8
	s_waitcnt vmcnt(20)
	v_mul_f32_e32 v12, 0x42800000, v12
	v_cvt_pk_fp8_f32 v174, v104, v124 op_sel:[0,0,1]
	v_cvt_pk_fp8_f32 v175, v72, v76 op_sel:[0,0,1]
	v_cvt_pk_fp8_f32 v176, v40, v44 op_sel:[0,0,1]
	v_cvt_pk_fp8_f32 v177, v8, v12 op_sel:[0,0,1]
	v_mul_f32_e32 v0, 0x42800000, v97
	v_mul_f32_e32 v4, 0x42800000, v101
	v_mul_f32_e32 v8, 0x42800000, v105
	ds_write_b128 v204, v[174:177] offset:32768
	v_mov_b32_e32 v174, v129
	v_cvt_pk_fp8_f32 v174, v0, v4
	v_mul_f32_e32 v0, 0x42800000, v65
	v_mul_f32_e32 v4, 0x42800000, v69
	v_mov_b32_e32 v175, v129
	v_cvt_pk_fp8_f32 v175, v0, v4
	v_mul_f32_e32 v0, 0x42800000, v33
	v_mul_f32_e32 v4, 0x42800000, v37
	v_mov_b32_e32 v176, v129
	v_cvt_pk_fp8_f32 v176, v0, v4
	v_mul_f32_e32 v0, 0x42800000, v1
	v_mul_f32_e32 v1, 0x42800000, v5
	v_mov_b32_e32 v177, v129
	v_cvt_pk_fp8_f32 v177, v0, v1
	v_mul_f32_e32 v12, 0x42800000, v125
	v_cvt_pk_fp8_f32 v174, v8, v12 op_sel:[0,0,1]
	v_mul_f32_e32 v8, 0x42800000, v73
	v_mul_f32_e32 v12, 0x42800000, v77
	v_cvt_pk_fp8_f32 v175, v8, v12 op_sel:[0,0,1]
	v_mul_f32_e32 v8, 0x42800000, v41
	v_mul_f32_e32 v12, 0x42800000, v45
	v_mul_f32_e32 v4, 0x42800000, v9
	v_mul_f32_e32 v5, 0x42800000, v13
	v_cvt_pk_fp8_f32 v176, v8, v12 op_sel:[0,0,1]
	v_cvt_pk_fp8_f32 v177, v4, v5 op_sel:[0,0,1]
	v_mul_f32_e32 v0, 0x42800000, v98
	v_mul_f32_e32 v1, 0x42800000, v102
	v_mul_f32_e32 v4, 0x42800000, v106
	ds_write_b128 v204, v[174:177] offset:32896
	v_mov_b32_e32 v174, v129
	v_cvt_pk_fp8_f32 v174, v0, v1
	v_mul_f32_e32 v0, 0x42800000, v66
	v_mul_f32_e32 v1, 0x42800000, v70
	v_mov_b32_e32 v175, v129
	v_cvt_pk_fp8_f32 v175, v0, v1
	v_mul_f32_e32 v0, 0x42800000, v34
	v_mul_f32_e32 v1, 0x42800000, v38
	v_mov_b32_e32 v176, v129
	v_cvt_pk_fp8_f32 v176, v0, v1
	v_mul_f32_e32 v0, 0x42800000, v2
	v_mul_f32_e32 v1, 0x42800000, v6
	v_mov_b32_e32 v177, v129
	v_mul_f32_e32 v5, 0x42800000, v126
	v_cvt_pk_fp8_f32 v177, v0, v1
	v_cvt_pk_fp8_f32 v174, v4, v5 op_sel:[0,0,1]
	v_mul_f32_e32 v4, 0x42800000, v74
	v_mul_f32_e32 v5, 0x42800000, v78
	v_cvt_pk_fp8_f32 v175, v4, v5 op_sel:[0,0,1]
	v_mul_f32_e32 v4, 0x42800000, v42
	v_mul_f32_e32 v5, 0x42800000, v46
	v_cvt_pk_fp8_f32 v176, v4, v5 op_sel:[0,0,1]
	v_mul_f32_e32 v2, 0x42800000, v10
	v_mul_f32_e32 v4, 0x42800000, v14
	v_cvt_pk_fp8_f32 v177, v2, v4 op_sel:[0,0,1]
	v_mul_f32_e32 v1, 0x42800000, v99
	v_mul_f32_e32 v2, 0x42800000, v103
	v_mov_b32_e32 v0, v129
	v_cvt_pk_fp8_f32 v0, v1, v2
	v_mul_f32_e32 v4, 0x42800000, v107
	v_mul_f32_e32 v5, 0x42800000, v127
	v_mul_f32_e32 v2, 0x42800000, v67
	v_cvt_pk_fp8_f32 v0, v4, v5 op_sel:[0,0,1]
	v_mul_f32_e32 v4, 0x42800000, v71
	v_mov_b32_e32 v1, v129
	v_cvt_pk_fp8_f32 v1, v2, v4
	v_mul_f32_e32 v5, 0x42800000, v75
	v_mul_f32_e32 v6, 0x42800000, v79
	v_mul_f32_e32 v4, 0x42800000, v35
	v_cvt_pk_fp8_f32 v1, v5, v6 op_sel:[0,0,1]
	v_mul_f32_e32 v5, 0x42800000, v39
	v_mov_b32_e32 v2, v129
	v_cvt_pk_fp8_f32 v2, v4, v5
	v_mul_f32_e32 v4, 0x42800000, v3
	v_mul_f32_e32 v5, 0x42800000, v7
	v_mov_b32_e32 v3, v129
	v_cvt_pk_fp8_f32 v3, v4, v5
	v_mul_f32_e32 v6, 0x42800000, v43
	v_mul_f32_e32 v8, 0x42800000, v47
	v_cvt_pk_fp8_f32 v2, v6, v8 op_sel:[0,0,1]
	v_mul_f32_e32 v6, 0x42800000, v11
	v_mul_f32_e32 v7, 0x42800000, v15
	v_cvt_pk_fp8_f32 v3, v6, v7 op_sel:[0,0,1]
	ds_write_b128 v204, v[174:177] offset:33024
	ds_write_b128 v204, v[0:3] offset:33152
	s_waitcnt lgkmcnt(0)
	s_barrier
; #define LAS __attribute__((address_space(3)))
; __device__ __forceinline__ unsigned pack4_fp8(float a, float b, float c, float d) { int r = 0; r = __builtin_amdgcn_cvt_pk_fp8_f32(a, b, r, false); r = __builtin_amdgcn_cvt_pk_fp8_f32(c, d, r, true); return (unsigned)r; }
; __device__ __forceinline__ void cvt8_to_lds(const f32x4 (&v)[16], LAS unsigned char* tile, int lane, int wv) {
; #pragma unroll
;     for (int i = 0; i < 4; ++i) { u32x4 w; w.x = pack4_fp8(v[0][i] * W8_SCALE, v[1][i] * W8_SCALE, v[2][i] * W8_SCALE, v[3][i] * W8_SCALE); w.y = pack4_fp8(v[4][i] * W8_SCALE, v[5][i] * W8_SCALE, v[6][i] * W8_SCALE, v[7][i] * W8_SCALE);
;         w.z = pack4_fp8(v[8][i] * W8_SCALE, v[9][i] * W8_SCALE, v[10][i] * W8_SCALE, v[11][i] * W8_SCALE); w.w = pack4_fp8(v[12][i] * W8_SCALE, v[13][i] * W8_SCALE, v[14][i] * W8_SCALE, v[15][i] * W8_SCALE);
;         *(LAS u32x4*)(tile + (4 * lane + i) * 128 + ((wv ^ (lane & 7)) << 4)) = w; }
; }
; __device__ __forceinline__ void cvt8_from_lds(const LAS unsigned char* tile, fp8_t* d, int ld_dst, int tid) {
;     const int c = tid & 7;
; #pragma unroll
;     for (int q = 0; q < 4; ++q) { const int r = (tid >> 3) + 64 * q; const u32x4 w = *(const LAS u32x4*)(tile + r * 128 + ((c ^ ((r >> 2) & 7)) << 4));
;         __builtin_nontemporal_store(w, (u32x4*)(d + (size_t)r * ld_dst + 16 * c)); }
; }
; __device__ __forceinline__ void cvt_item_lds(const float* src, int ld_src, fp8_t* dst, int ld_dst, LAS unsigned char* lds, int tid, int wv) {
;     const int lane = tid & 63;
;     const float* s = src + (size_t)(16 * wv) * ld_src + 4 * lane;
;     f32x4 va[16], vb[16];
;     cvt8_load(va, s, ld_src);
; #pragma unroll
;     for (int t = 0; t < 8; t += 2) {
;         cvt8_load(vb, s + (t + 1) * 256, ld_src); __builtin_amdgcn_sched_barrier(0);
;         cvt8_to_lds(va, lds, lane, wv); CVT_LDS_BAR(); __builtin_amdgcn_sched_barrier(0);
;         cvt8_from_lds(lds, dst + (size_t)(t * 256) * ld_dst, ld_dst, tid); __builtin_amdgcn_sched_barrier(0);
;         if (t + 2 < 8) { cvt8_load(va, s + (t + 2) * 256, ld_src); __builtin_amdgcn_sched_barrier(0); }
;         cvt8_to_lds(vb, lds + 32768, lane, wv); CVT_LDS_BAR(); __builtin_amdgcn_sched_barrier(0);
;         cvt8_from_lds(lds + 32768, dst + (size_t)((t + 1) * 256) * ld_dst, ld_dst, tid); __builtin_amdgcn_sched_barrier(0);
;     }
	ds_read_b128 v[0:3], v205 offset:32768
	v_lshl_add_u64 v[4:5], v[140:141], 0, s[42:43]
	v_lshl_add_u64 v[6:7], v[4:5], 0, v[132:133]
	s_waitcnt lgkmcnt(0)
	global_store_dwordx4 v[6:7], v[0:3], off nt
	ds_read_b128 v[0:3], v206 offset:32768
	v_lshl_add_u64 v[6:7], v[4:5], 0, v[134:135]
	s_waitcnt lgkmcnt(0)
	global_store_dwordx4 v[6:7], v[0:3], off nt
	ds_read_b128 v[0:3], v207 offset:32768
	v_lshl_add_u64 v[6:7], v[4:5], 0, v[136:137]
	v_lshl_add_u64 v[4:5], v[4:5], 0, v[138:139]
	s_waitcnt lgkmcnt(0)
	global_store_dwordx4 v[6:7], v[0:3], off nt
	ds_read_b128 v[0:3], v208 offset:32768
	s_waitcnt lgkmcnt(0)
	global_store_dwordx4 v[4:5], v[0:3], off nt
	global_load_dwordx4 v[96:99], v[172:173], off offset:3072 nt
	global_load_dwordx4 v[100:103], v[142:143], off offset:3072 nt
	global_load_dwordx4 v[104:107], v[144:145], off offset:3072 nt
	global_load_dwordx4 v[124:127], v[146:147], off offset:3072 nt
	global_load_dwordx4 v[64:67], v[148:149], off offset:3072 nt
	global_load_dwordx4 v[68:71], v[150:151], off offset:3072 nt
	global_load_dwordx4 v[72:75], v[152:153], off offset:3072 nt
	global_load_dwordx4 v[76:79], v[154:155], off offset:3072 nt
	global_load_dwordx4 v[32:35], v[156:157], off offset:3072 nt
	global_load_dwordx4 v[36:39], v[158:159], off offset:3072 nt
	global_load_dwordx4 v[40:43], v[160:161], off offset:3072 nt
	global_load_dwordx4 v[44:47], v[162:163], off offset:3072 nt
	global_load_dwordx4 v[0:3], v[164:165], off offset:3072 nt
	global_load_dwordx4 v[4:7], v[166:167], off offset:3072 nt
	global_load_dwordx4 v[8:11], v[168:169], off offset:3072 nt
	global_load_dwordx4 v[12:15], v[170:171], off offset:3072 nt
	s_waitcnt vmcnt(35)
	v_mul_f32_e32 v108, 0x42800000, v108
	s_waitcnt vmcnt(34)
	v_mul_f32_e32 v112, 0x42800000, v112
	v_mov_b32_e32 v142, v129
	s_waitcnt vmcnt(31)
	v_mul_f32_e32 v80, 0x42800000, v80
	s_waitcnt vmcnt(30)
	v_mul_f32_e32 v84, 0x42800000, v84
	v_mov_b32_e32 v143, v129
	s_waitcnt vmcnt(27)
	v_mul_f32_e32 v48, 0x42800000, v48
	s_waitcnt vmcnt(26)
	v_mul_f32_e32 v52, 0x42800000, v52
	v_mov_b32_e32 v144, v129
	s_waitcnt vmcnt(23)
	v_mul_f32_e32 v16, 0x42800000, v16
	s_waitcnt vmcnt(22)
	v_mul_f32_e32 v20, 0x42800000, v20
	v_mov_b32_e32 v145, v129
	v_cvt_pk_fp8_f32 v142, v108, v112
	v_cvt_pk_fp8_f32 v143, v80, v84
	v_cvt_pk_fp8_f32 v144, v48, v52
	v_cvt_pk_fp8_f32 v145, v16, v20
	v_mul_f32_e32 v116, 0x42800000, v116
	v_mul_f32_e32 v120, 0x42800000, v120
	v_mul_f32_e32 v88, 0x42800000, v88
	v_mul_f32_e32 v92, 0x42800000, v92
	v_mul_f32_e32 v56, 0x42800000, v56
	v_mul_f32_e32 v60, 0x42800000, v60
	s_waitcnt vmcnt(21)
	v_mul_f32_e32 v24, 0x42800000, v24
	s_waitcnt vmcnt(20)
	v_mul_f32_e32 v28, 0x42800000, v28
	v_cvt_pk_fp8_f32 v142, v116, v120 op_sel:[0,0,1]
	v_cvt_pk_fp8_f32 v143, v88, v92 op_sel:[0,0,1]
	v_cvt_pk_fp8_f32 v144, v56, v60 op_sel:[0,0,1]
	v_cvt_pk_fp8_f32 v145, v24, v28 op_sel:[0,0,1]
	v_mul_f32_e32 v16, 0x42800000, v109
	v_mul_f32_e32 v20, 0x42800000, v113
	v_mul_f32_e32 v24, 0x42800000, v117
	ds_write_b128 v204, v[142:145]
	v_mov_b32_e32 v142, v129
	v_cvt_pk_fp8_f32 v142, v16, v20
	v_mul_f32_e32 v16, 0x42800000, v81
	v_mul_f32_e32 v20, 0x42800000, v85
	v_mov_b32_e32 v143, v129
	v_cvt_pk_fp8_f32 v143, v16, v20
	v_mul_f32_e32 v16, 0x42800000, v49
	v_mul_f32_e32 v20, 0x42800000, v53
	v_mov_b32_e32 v144, v129
	v_cvt_pk_fp8_f32 v144, v16, v20
	v_mul_f32_e32 v16, 0x42800000, v17
	v_mul_f32_e32 v17, 0x42800000, v21
	v_mov_b32_e32 v145, v129
	v_cvt_pk_fp8_f32 v145, v16, v17
	v_mul_f32_e32 v28, 0x42800000, v121
	v_cvt_pk_fp8_f32 v142, v24, v28 op_sel:[0,0,1]
	v_mul_f32_e32 v24, 0x42800000, v89
	v_mul_f32_e32 v28, 0x42800000, v93
	v_cvt_pk_fp8_f32 v143, v24, v28 op_sel:[0,0,1]
	v_mul_f32_e32 v24, 0x42800000, v57
	v_mul_f32_e32 v28, 0x42800000, v61
	v_mul_f32_e32 v20, 0x42800000, v25
	v_mul_f32_e32 v21, 0x42800000, v29
	v_cvt_pk_fp8_f32 v144, v24, v28 op_sel:[0,0,1]
	v_cvt_pk_fp8_f32 v145, v20, v21 op_sel:[0,0,1]
	v_mul_f32_e32 v16, 0x42800000, v110
	v_mul_f32_e32 v17, 0x42800000, v114
	v_mul_f32_e32 v20, 0x42800000, v118
	ds_write_b128 v204, v[142:145] offset:128
	v_mov_b32_e32 v142, v129
	v_cvt_pk_fp8_f32 v142, v16, v17
	v_mul_f32_e32 v16, 0x42800000, v82
	v_mul_f32_e32 v17, 0x42800000, v86
	v_mov_b32_e32 v143, v129
	v_cvt_pk_fp8_f32 v143, v16, v17
	v_mul_f32_e32 v16, 0x42800000, v50
	v_mul_f32_e32 v17, 0x42800000, v54
	v_mov_b32_e32 v144, v129
	v_cvt_pk_fp8_f32 v144, v16, v17
	v_mul_f32_e32 v16, 0x42800000, v18
	v_mul_f32_e32 v17, 0x42800000, v22
	v_mov_b32_e32 v145, v129
	v_mul_f32_e32 v21, 0x42800000, v122
	v_cvt_pk_fp8_f32 v145, v16, v17
	v_cvt_pk_fp8_f32 v142, v20, v21 op_sel:[0,0,1]
	v_mul_f32_e32 v20, 0x42800000, v90
	v_mul_f32_e32 v21, 0x42800000, v94
	v_cvt_pk_fp8_f32 v143, v20, v21 op_sel:[0,0,1]
	v_mul_f32_e32 v20, 0x42800000, v58
	v_mul_f32_e32 v21, 0x42800000, v62
	v_cvt_pk_fp8_f32 v144, v20, v21 op_sel:[0,0,1]
	v_mul_f32_e32 v18, 0x42800000, v26
	v_mul_f32_e32 v20, 0x42800000, v30
	v_cvt_pk_fp8_f32 v145, v18, v20 op_sel:[0,0,1]
	v_mul_f32_e32 v17, 0x42800000, v111
	v_mul_f32_e32 v18, 0x42800000, v115
	v_mov_b32_e32 v16, v129
	v_cvt_pk_fp8_f32 v16, v17, v18
	v_mul_f32_e32 v20, 0x42800000, v119
	v_mul_f32_e32 v21, 0x42800000, v123
	v_mul_f32_e32 v18, 0x42800000, v83
	v_cvt_pk_fp8_f32 v16, v20, v21 op_sel:[0,0,1]
	v_mul_f32_e32 v20, 0x42800000, v87
	v_mov_b32_e32 v17, v129
	v_cvt_pk_fp8_f32 v17, v18, v20
	v_mul_f32_e32 v21, 0x42800000, v91
	v_mul_f32_e32 v22, 0x42800000, v95
	v_mul_f32_e32 v20, 0x42800000, v51
	v_cvt_pk_fp8_f32 v17, v21, v22 op_sel:[0,0,1]
	v_mul_f32_e32 v21, 0x42800000, v55
	v_mov_b32_e32 v18, v129
	v_cvt_pk_fp8_f32 v18, v20, v21
	v_mul_f32_e32 v20, 0x42800000, v19
	v_mul_f32_e32 v21, 0x42800000, v23
	v_mov_b32_e32 v19, v129
	v_cvt_pk_fp8_f32 v19, v20, v21
	v_mul_f32_e32 v22, 0x42800000, v59
	v_mul_f32_e32 v24, 0x42800000, v63
	v_cvt_pk_fp8_f32 v18, v22, v24 op_sel:[0,0,1]
	v_mul_f32_e32 v22, 0x42800000, v27
	v_mul_f32_e32 v23, 0x42800000, v31
	v_cvt_pk_fp8_f32 v19, v22, v23 op_sel:[0,0,1]
	ds_write_b128 v204, v[142:145] offset:256
	ds_write_b128 v204, v[16:19] offset:384
	s_waitcnt lgkmcnt(0)
	s_barrier
; #define LAS __attribute__((address_space(3)))
; __device__ __forceinline__ unsigned pack4_fp8(float a, float b, float c, float d) { int r = 0; r = __builtin_amdgcn_cvt_pk_fp8_f32(a, b, r, false); r = __builtin_amdgcn_cvt_pk_fp8_f32(c, d, r, true); return (unsigned)r; }
; __device__ __forceinline__ void cvt8_to_lds(const f32x4 (&v)[16], LAS unsigned char* tile, int lane, int wv) {
; #pragma unroll
;     for (int i = 0; i < 4; ++i) { u32x4 w; w.x = pack4_fp8(v[0][i] * W8_SCALE, v[1][i] * W8_SCALE, v[2][i] * W8_SCALE, v[3][i] * W8_SCALE); w.y = pack4_fp8(v[4][i] * W8_SCALE, v[5][i] * W8_SCALE, v[6][i] * W8_SCALE, v[7][i] * W8_SCALE);
;         w.z = pack4_fp8(v[8][i] * W8_SCALE, v[9][i] * W8_SCALE, v[10][i] * W8_SCALE, v[11][i] * W8_SCALE); w.w = pack4_fp8(v[12][i] * W8_SCALE, v[13][i] * W8_SCALE, v[14][i] * W8_SCALE, v[15][i] * W8_SCALE);
;         *(LAS u32x4*)(tile + (4 * lane + i) * 128 + ((wv ^ (lane & 7)) << 4)) = w; }
; }
; __device__ __forceinline__ void cvt8_from_lds(const LAS unsigned char* tile, fp8_t* d, int ld_dst, int tid) {
;     const int c = tid & 7;
; #pragma unroll
;     for (int q = 0; q < 4; ++q) { const int r = (tid >> 3) + 64 * q; const u32x4 w = *(const LAS u32x4*)(tile + r * 128 + ((c ^ ((r >> 2) & 7)) << 4));
;         __builtin_nontemporal_store(w, (u32x4*)(d + (size_t)r * ld_dst + 16 * c)); }
; }
; __device__ __forceinline__ void cvt_item_lds(const float* src, int ld_src, fp8_t* dst, int ld_dst, LAS unsigned char* lds, int tid, int wv) {
;     const int lane = tid & 63;
;     const float* s = src + (size_t)(16 * wv) * ld_src + 4 * lane;
;     f32x4 va[16], vb[16];
;     cvt8_load(va, s, ld_src);
; #pragma unroll
;     for (int t = 0; t < 8; t += 2) {
;         cvt8_load(vb, s + (t + 1) * 256, ld_src); __builtin_amdgcn_sched_barrier(0);
;         cvt8_to_lds(va, lds, lane, wv); CVT_LDS_BAR(); __builtin_amdgcn_sched_barrier(0);
;         cvt8_from_lds(lds, dst + (size_t)(t * 256) * ld_dst, ld_dst, tid); __builtin_amdgcn_sched_barrier(0);
;         if (t + 2 < 8) { cvt8_load(va, s + (t + 2) * 256, ld_src); __builtin_amdgcn_sched_barrier(0); }
;         cvt8_to_lds(vb, lds + 32768, lane, wv); CVT_LDS_BAR(); __builtin_amdgcn_sched_barrier(0);
;         cvt8_from_lds(lds + 32768, dst + (size_t)((t + 1) * 256) * ld_dst, ld_dst, tid); __builtin_amdgcn_sched_barrier(0);
;     }
	ds_read_b128 v[16:19], v205
	v_lshl_add_u64 v[20:21], v[140:141], 0, s[44:45]
	v_lshl_add_u64 v[22:23], v[20:21], 0, v[132:133]
	s_waitcnt lgkmcnt(0)
	global_store_dwordx4 v[22:23], v[16:19], off nt
	ds_read_b128 v[16:19], v206
	v_lshl_add_u64 v[22:23], v[20:21], 0, v[134:135]
	s_waitcnt lgkmcnt(0)
	global_store_dwordx4 v[22:23], v[16:19], off nt
	ds_read_b128 v[16:19], v207
	v_lshl_add_u64 v[22:23], v[20:21], 0, v[136:137]
	v_lshl_add_u64 v[20:21], v[20:21], 0, v[138:139]
	s_waitcnt lgkmcnt(0)
	global_store_dwordx4 v[22:23], v[16:19], off nt
	ds_read_b128 v[16:19], v208
	s_waitcnt lgkmcnt(0)
	global_store_dwordx4 v[20:21], v[16:19], off nt
	s_waitcnt vmcnt(19)
	s_nop 0
	v_mul_f32_e32 v17, 0x42800000, v96
	s_waitcnt vmcnt(18)
	v_mul_f32_e32 v18, 0x42800000, v100
	v_mov_b32_e32 v16, v129
	v_cvt_pk_fp8_f32 v16, v17, v18
	s_waitcnt vmcnt(17)
	v_mul_f32_e32 v19, 0x42800000, v104
	s_waitcnt vmcnt(16)
	v_mul_f32_e32 v20, 0x42800000, v124
	s_waitcnt vmcnt(15)
	v_mul_f32_e32 v18, 0x42800000, v64
	v_cvt_pk_fp8_f32 v16, v19, v20 op_sel:[0,0,1]
	s_waitcnt vmcnt(14)
	v_mul_f32_e32 v19, 0x42800000, v68
	v_mov_b32_e32 v17, v129
	v_cvt_pk_fp8_f32 v17, v18, v19
	s_waitcnt vmcnt(13)
	v_mul_f32_e32 v20, 0x42800000, v72
	s_waitcnt vmcnt(12)
	v_mul_f32_e32 v21, 0x42800000, v76
	s_waitcnt vmcnt(11)
	v_mul_f32_e32 v19, 0x42800000, v32
	v_cvt_pk_fp8_f32 v17, v20, v21 op_sel:[0,0,1]
	s_waitcnt vmcnt(10)
	v_mul_f32_e32 v20, 0x42800000, v36
	v_mov_b32_e32 v18, v129
	v_cvt_pk_fp8_f32 v18, v19, v20
	s_waitcnt vmcnt(7)
	v_mul_f32_e32 v0, 0x42800000, v0
	s_waitcnt vmcnt(6)
	v_mul_f32_e32 v4, 0x42800000, v4
	v_mov_b32_e32 v19, v129
	v_cvt_pk_fp8_f32 v19, v0, v4
	v_mul_f32_e32 v21, 0x42800000, v40
	v_mul_f32_e32 v22, 0x42800000, v44
	s_waitcnt vmcnt(5)
	v_mul_f32_e32 v8, 0x42800000, v8
	s_waitcnt vmcnt(4)
	v_mul_f32_e32 v12, 0x42800000, v12
	v_cvt_pk_fp8_f32 v18, v21, v22 op_sel:[0,0,1]
	v_cvt_pk_fp8_f32 v19, v8, v12 op_sel:[0,0,1]
	v_mul_f32_e32 v0, 0x42800000, v97
	v_mul_f32_e32 v4, 0x42800000, v101
	v_mul_f32_e32 v8, 0x42800000, v105
	ds_write_b128 v204, v[16:19] offset:32768
	v_mov_b32_e32 v16, v129
	v_cvt_pk_fp8_f32 v16, v0, v4
	v_mul_f32_e32 v0, 0x42800000, v65
	v_mul_f32_e32 v4, 0x42800000, v69
	v_mov_b32_e32 v17, v129
	v_cvt_pk_fp8_f32 v17, v0, v4
	v_mul_f32_e32 v0, 0x42800000, v33
	v_mul_f32_e32 v4, 0x42800000, v37
	v_mov_b32_e32 v18, v129
	v_cvt_pk_fp8_f32 v18, v0, v4
	v_mul_f32_e32 v0, 0x42800000, v1
	v_mul_f32_e32 v1, 0x42800000, v5
	v_mov_b32_e32 v19, v129
	v_cvt_pk_fp8_f32 v19, v0, v1
	v_mul_f32_e32 v12, 0x42800000, v125
	v_cvt_pk_fp8_f32 v16, v8, v12 op_sel:[0,0,1]
	v_mul_f32_e32 v8, 0x42800000, v73
	v_mul_f32_e32 v12, 0x42800000, v77
	v_cvt_pk_fp8_f32 v17, v8, v12 op_sel:[0,0,1]
	v_mul_f32_e32 v8, 0x42800000, v41
	v_mul_f32_e32 v12, 0x42800000, v45
	v_mul_f32_e32 v4, 0x42800000, v9
	v_mul_f32_e32 v5, 0x42800000, v13
	v_cvt_pk_fp8_f32 v18, v8, v12 op_sel:[0,0,1]
	v_cvt_pk_fp8_f32 v19, v4, v5 op_sel:[0,0,1]
	v_mul_f32_e32 v0, 0x42800000, v98
	v_mul_f32_e32 v1, 0x42800000, v102
	v_mul_f32_e32 v4, 0x42800000, v106
	ds_write_b128 v204, v[16:19] offset:32896
	v_mov_b32_e32 v16, v129
	v_cvt_pk_fp8_f32 v16, v0, v1
	v_mul_f32_e32 v0, 0x42800000, v66
	v_mul_f32_e32 v1, 0x42800000, v70
	v_mov_b32_e32 v17, v129
	v_cvt_pk_fp8_f32 v17, v0, v1
	v_mul_f32_e32 v0, 0x42800000, v34
	v_mul_f32_e32 v1, 0x42800000, v38
	v_mov_b32_e32 v18, v129
	v_cvt_pk_fp8_f32 v18, v0, v1
	v_mul_f32_e32 v0, 0x42800000, v2
	v_mul_f32_e32 v1, 0x42800000, v6
	v_mov_b32_e32 v19, v129
	v_mul_f32_e32 v5, 0x42800000, v126
	v_cvt_pk_fp8_f32 v19, v0, v1
	v_cvt_pk_fp8_f32 v16, v4, v5 op_sel:[0,0,1]
	v_mul_f32_e32 v4, 0x42800000, v74
	v_mul_f32_e32 v5, 0x42800000, v78
	v_cvt_pk_fp8_f32 v17, v4, v5 op_sel:[0,0,1]
	v_mul_f32_e32 v4, 0x42800000, v42
	v_mul_f32_e32 v5, 0x42800000, v46
	v_cvt_pk_fp8_f32 v18, v4, v5 op_sel:[0,0,1]
	v_mul_f32_e32 v2, 0x42800000, v10
	v_mul_f32_e32 v4, 0x42800000, v14
	v_cvt_pk_fp8_f32 v19, v2, v4 op_sel:[0,0,1]
	v_mul_f32_e32 v1, 0x42800000, v99
	v_mul_f32_e32 v2, 0x42800000, v103
	v_mov_b32_e32 v0, v129
	v_cvt_pk_fp8_f32 v0, v1, v2
	v_mul_f32_e32 v4, 0x42800000, v107
	v_mul_f32_e32 v5, 0x42800000, v127
	v_mul_f32_e32 v2, 0x42800000, v67
	v_cvt_pk_fp8_f32 v0, v4, v5 op_sel:[0,0,1]
	v_mul_f32_e32 v4, 0x42800000, v71
	v_mov_b32_e32 v1, v129
	v_cvt_pk_fp8_f32 v1, v2, v4
	v_mul_f32_e32 v5, 0x42800000, v75
	v_mul_f32_e32 v6, 0x42800000, v79
	v_mul_f32_e32 v4, 0x42800000, v35
	v_cvt_pk_fp8_f32 v1, v5, v6 op_sel:[0,0,1]
	v_mul_f32_e32 v5, 0x42800000, v39
	v_mov_b32_e32 v2, v129
	v_cvt_pk_fp8_f32 v2, v4, v5
	v_mul_f32_e32 v4, 0x42800000, v3
	v_mul_f32_e32 v5, 0x42800000, v7
	v_mov_b32_e32 v3, v129
	v_cvt_pk_fp8_f32 v3, v4, v5
	v_mul_f32_e32 v6, 0x42800000, v43
	v_mul_f32_e32 v8, 0x42800000, v47
	v_cvt_pk_fp8_f32 v2, v6, v8 op_sel:[0,0,1]
	v_mul_f32_e32 v6, 0x42800000, v11
	v_mul_f32_e32 v7, 0x42800000, v15
	v_cvt_pk_fp8_f32 v3, v6, v7 op_sel:[0,0,1]
	ds_write_b128 v204, v[16:19] offset:33024
	ds_write_b128 v204, v[0:3] offset:33152
	s_waitcnt lgkmcnt(0)
	s_barrier
	ds_read_b128 v[0:3], v205 offset:32768
	v_lshl_add_u64 v[4:5], v[140:141], 0, s[46:47]
	v_lshl_add_u64 v[6:7], v[4:5], 0, v[132:133]
	s_waitcnt lgkmcnt(0)
	global_store_dwordx4 v[6:7], v[0:3], off nt
	ds_read_b128 v[0:3], v206 offset:32768
	v_lshl_add_u64 v[6:7], v[4:5], 0, v[134:135]
	s_waitcnt lgkmcnt(0)
	global_store_dwordx4 v[6:7], v[0:3], off nt
	ds_read_b128 v[0:3], v207 offset:32768
	v_lshl_add_u64 v[6:7], v[4:5], 0, v[136:137]
	v_lshl_add_u64 v[4:5], v[4:5], 0, v[138:139]
	s_waitcnt lgkmcnt(0)
	global_store_dwordx4 v[6:7], v[0:3], off nt
	ds_read_b128 v[0:3], v208 offset:32768
	s_waitcnt lgkmcnt(0)
	global_store_dwordx4 v[4:5], v[0:3], off nt
	s_mov_b64 s[48:49], 0

; __device__ __forceinline__ void conv_queue(const Params& p, LAS unsigned char* lds, const int wave, const int cw, const int first, const int last, const int slot_off = LDS_MISC) {
;     ...
;         if (tid == 0) *slot = first + (int)atomicAdd(&p.ctl[cw], 1u);
;         __syncthreads();
;         const int it = *slot;
; __global__ void __launch_bounds__(NTHREADS, 2) fwd(Params p) {
;     ...
;         if (bid < NCV) conv_queue(p, lds, wave, CW_CONV4, N_GU + XP5, N_GU + N_DN - N_DEFER, LDS_MISC + 1024);
.LBB0_1251:
	s_or_b64 exec, exec, s[52:53]
	s_waitcnt vmcnt(0)
	v_readfirstlane_b32 s2, v1
	v_mov_b32_e32 v1, s13
	s_nop 0
	v_add_u32_e32 v0, s2, v0
	v_add_u32_e32 v0, 0x440, v0
	ds_write_b32 v1, v0

; __device__ __forceinline__ void conv_queue(const Params& p, LAS unsigned char* lds, const int wave, const int cw, const int first, const int last, const int slot_off = LDS_MISC) {
;     ...
;         if (tid == 0) *slot = first + (int)atomicAdd(&p.ctl[cw], 1u);
;         __syncthreads();
;         const int it = *slot;
; __global__ void __launch_bounds__(NTHREADS, 2) fwd(Params p) {
;     ...
;     conv_queue(p, lds, wave, CW_CONV4, N_GU + XP5, N_GU + N_DN - N_DEFER, LDS_MISC + 1024);
.LBB0_1276:
	s_or_b64 exec, exec, s[50:51]
	s_waitcnt vmcnt(0)
	v_readfirstlane_b32 s2, v1
	v_mov_b32_e32 v1, s13
	s_nop 0
	v_add_u32_e32 v0, s2, v0
	v_add_u32_e32 v0, 0x440, v0
	ds_write_b32 v1, v0
